# A/B: per-phase s_setprio flips removed from the five GEMM main loops (timing only)
# baseline (speedup 1.0000x reference)
; #define PG8_STAGE(bufoff, gbase, voff) do { _Pragma("unroll") for (int _i = 0; _i < 2; ++_i) \
;         __builtin_amdgcn_raw_ptr_buffer_load_lds(rsrc, (LAS void*)(lds + (bufoff) + ldsw + _i * 8192), 16, (int)(voff)[_i], (int)(gbase), 0, 0); } while (0)
; #define PG8_STAGE_A(bufoff, h, goff) do { if constexpr (GATHER) { PG8_STAGE(bufoff, goff, vG[h]); } else { PG8_STAGE(bufoff, (goff) + (h) * hstep, voffA); } } while (0)
; #define PG8_WAIT_V(n) asm volatile("s_waitcnt vmcnt(" #n ")" ::: "memory")
; #define PG8_WAIT_L(n) asm volatile("s_waitcnt lgkmcnt(" #n ")" ::: "memory")
; #define PG8_BAR __builtin_amdgcn_s_barrier()
; #define PG8_SCHED __builtin_amdgcn_sched_barrier(0)
;     DI int row_cnt(const pg8::Unit& u) const { return __builtin_amdgcn_readfirstlane(tab[u.a0]) - u.ldc; }
;     ...
;             PG8_LDB(B0, 0, 0); PG8_LDB(B1, 0, 1); PG8_SCHED; PG8_LDA(At, 0, 0); PG8_STAGE_A(PG8_SA(1, 1), 1, a1);
;             if constexpr (GATHER) { if (last && has_next) load_rows((ui + 1) & 1, S.row_cnt(nxt)); }
;             PG8_WAIT_V(8); PG8_WAIT_L(0); PG8_BAR; PG8_MMA(0, 0, At, B0); PG8_MMA(0, 1, At, B1); PG8_BAR; PG8_SCHED;
;             PG8_LDA(At, 0, 1); PG8_STAGE(PG8_SB(0, 0), b2, voffB); PG8_STAGE(PG8_SB(0, 1), b2 + hstep, voffB); PG8_STAGE_A(PG8_SA(0, 0), 0, a2);
;             PG8_WAIT_V(8); PG8_WAIT_L(0); PG8_BAR; PG8_MMA(1, 0, At, B0); PG8_MMA(1, 1, At, B1); PG8_BAR; PG8_SCHED;
;             PG8_LDB(B0, 1, 0); PG8_LDB(B1, 1, 1); PG8_SCHED; PG8_LDA(At, 1, 0); PG8_STAGE_A(PG8_SA(0, 1), 1, a2);
;             PG8_WAIT_V(8); PG8_WAIT_L(0); PG8_BAR; PG8_MMA(0, 0, At, B0); PG8_MMA(0, 1, At, B1); PG8_BAR; PG8_SCHED;
;             PG8_LDA(At, 1, 1); PG8_STAGE(PG8_SB(1, 0), b3, voffB); PG8_STAGE(PG8_SB(1, 1), b3 + hstep, voffB); PG8_STAGE_A(PG8_SA(1, 0), 0, a3);
;             PG8_WAIT_V(8); PG8_WAIT_L(0); PG8_BAR; PG8_MMA(1, 0, At, B0); PG8_MMA(1, 1, At, B1); PG8_BAR; PG8_SCHED;
.LBB0_337:
	s_waitcnt vmcnt(4)
	ds_read_b128 v[64:67], v159
	s_waitcnt vmcnt(2)
	ds_read_b128 v[68:71], v160
	ds_read_b128 v[72:75], v161
	s_waitcnt vmcnt(1)
	ds_read_b128 v[76:79], v162
	ds_read_b128 v[144:147], v163
	ds_read_b128 v[148:151], v164
	ds_read_b128 v[174:177], v165
	ds_read_b128 v[178:181], v166
	s_add_i32 s4, s2, 0xfffc0080
	s_cmp_eq_u32 s10, 12
	s_cselect_b32 s53, s41, s4
	s_cselect_b32 s51, s82, s3
	s_add_i32 s50, s53, 0x80
	s_mov_b32 s4, s86
	s_mov_b32 m0, s74
	ds_read_b128 v[182:185], v167
	ds_read_b128 v[186:189], v167 offset:2048
	ds_read_b128 v[190:193], v168
	ds_read_b128 v[194:197], v168 offset:2048
	ds_read_b128 v[198:201], v167 offset:4096
	ds_read_b128 v[202:205], v167 offset:6144
	ds_read_b128 v[206:209], v168 offset:4096
	ds_read_b128 v[210:213], v168 offset:6144
	buffer_load_dwordx4 v153, s[4:7], s2 offen lds
	s_mov_b32 m0, s77
	s_nop 0
	buffer_load_dwordx4 v155, s[4:7], s2 offen lds
	s_waitcnt vmcnt(8)
	s_waitcnt lgkmcnt(0)
	s_barrier
	s_waitcnt lgkmcnt(7)
	v_mfma_i32_16x16x64_i8 v[60:63], v[64:67], v[182:185], v[60:63]
	v_mfma_i32_16x16x64_i8 v[56:59], v[72:75], v[182:185], v[56:59]
	s_waitcnt lgkmcnt(6)
	v_mfma_i32_16x16x64_i8 v[52:55], v[64:67], v[186:189], v[52:55]
	v_mfma_i32_16x16x64_i8 v[48:51], v[72:75], v[186:189], v[48:51]
	s_waitcnt lgkmcnt(3)
	v_mfma_i32_16x16x64_i8 v[44:47], v[64:67], v[198:201], v[44:47]
	v_mfma_i32_16x16x64_i8 v[40:43], v[72:75], v[198:201], v[40:43]
	s_waitcnt lgkmcnt(2)
	v_mfma_i32_16x16x64_i8 v[36:39], v[64:67], v[202:205], v[36:39]
	v_mfma_i32_16x16x64_i8 v[32:35], v[72:75], v[202:205], v[32:35]
	v_mfma_i32_16x16x64_i8 v[60:63], v[68:71], v[190:193], v[60:63]
	v_mfma_i32_16x16x64_i8 v[56:59], v[76:79], v[190:193], v[56:59]
	v_mfma_i32_16x16x64_i8 v[52:55], v[68:71], v[194:197], v[52:55]
	v_mfma_i32_16x16x64_i8 v[48:51], v[76:79], v[194:197], v[48:51]
	s_waitcnt lgkmcnt(1)
	v_mfma_i32_16x16x64_i8 v[44:47], v[68:71], v[206:209], v[44:47]
	v_mfma_i32_16x16x64_i8 v[40:43], v[76:79], v[206:209], v[40:43]
	s_waitcnt lgkmcnt(0)
	v_mfma_i32_16x16x64_i8 v[36:39], v[68:71], v[210:213], v[36:39]
	v_mfma_i32_16x16x64_i8 v[32:35], v[76:79], v[210:213], v[32:35]
	v_mfma_i32_16x16x64_i8 v[140:143], v[144:147], v[182:185], v[140:143]
	v_mfma_i32_16x16x64_i8 v[136:139], v[174:177], v[182:185], v[136:139]
	v_mfma_i32_16x16x64_i8 v[132:135], v[144:147], v[186:189], v[132:135]
	v_mfma_i32_16x16x64_i8 v[128:131], v[174:177], v[186:189], v[128:131]
	v_mfma_i32_16x16x64_i8 v[124:127], v[144:147], v[198:201], v[124:127]
	v_mfma_i32_16x16x64_i8 v[120:123], v[174:177], v[198:201], v[120:123]
	v_mfma_i32_16x16x64_i8 v[116:119], v[144:147], v[202:205], v[116:119]
	v_mfma_i32_16x16x64_i8 v[112:115], v[174:177], v[202:205], v[112:115]
	v_mfma_i32_16x16x64_i8 v[140:143], v[148:151], v[190:193], v[140:143]
	v_mfma_i32_16x16x64_i8 v[136:139], v[178:181], v[190:193], v[136:139]
	v_mfma_i32_16x16x64_i8 v[132:135], v[148:151], v[194:197], v[132:135]
	v_mfma_i32_16x16x64_i8 v[128:131], v[178:181], v[194:197], v[128:131]
	v_mfma_i32_16x16x64_i8 v[124:127], v[148:151], v[206:209], v[124:127]
	v_mfma_i32_16x16x64_i8 v[120:123], v[178:181], v[206:209], v[120:123]
	v_mfma_i32_16x16x64_i8 v[116:119], v[148:151], v[210:213], v[116:119]
	v_mfma_i32_16x16x64_i8 v[112:115], v[178:181], v[210:213], v[112:115]
	s_barrier
	s_mov_b32 m0, s57
	ds_read_b128 v[182:185], v167 offset:16384
	ds_read_b128 v[186:189], v167 offset:18432
	ds_read_b128 v[190:193], v168 offset:16384
	ds_read_b128 v[194:197], v168 offset:18432
	ds_read_b128 v[198:201], v167 offset:20480
	ds_read_b128 v[202:205], v167 offset:22528
	ds_read_b128 v[206:209], v168 offset:20480
	ds_read_b128 v[210:213], v168 offset:22528
	buffer_load_dwordx4 v154, s[4:7], s51 offen lds
	s_mov_b32 m0, s58
	s_add_i32 s54, s51, 0x40000
	buffer_load_dwordx4 v156, s[4:7], s51 offen lds
	s_mov_b32 m0, s59
	s_nop 0
	buffer_load_dwordx4 v154, s[4:7], s54 offen lds
	s_mov_b32 m0, s60
	s_nop 0
	buffer_load_dwordx4 v156, s[4:7], s54 offen lds
	s_mov_b32 m0, s56
	s_nop 0
	buffer_load_dwordx4 v153, s[4:7], s53 offen lds
	s_mov_b32 m0, s61
	s_nop 0
	buffer_load_dwordx4 v155, s[4:7], s53 offen lds
	s_waitcnt vmcnt(8)
	s_waitcnt lgkmcnt(0)
	s_barrier
	s_waitcnt lgkmcnt(7)
	v_mfma_i32_16x16x64_i8 v[28:31], v[64:67], v[182:185], v[28:31]
	v_mfma_i32_16x16x64_i8 v[24:27], v[72:75], v[182:185], v[24:27]
	s_waitcnt lgkmcnt(6)
	v_mfma_i32_16x16x64_i8 v[20:23], v[64:67], v[186:189], v[20:23]
	v_mfma_i32_16x16x64_i8 v[16:19], v[72:75], v[186:189], v[16:19]
	s_waitcnt lgkmcnt(3)
	v_mfma_i32_16x16x64_i8 v[12:15], v[64:67], v[198:201], v[12:15]
	v_mfma_i32_16x16x64_i8 v[8:11], v[72:75], v[198:201], v[8:11]
	s_waitcnt lgkmcnt(2)
	v_mfma_i32_16x16x64_i8 v[4:7], v[64:67], v[202:205], v[4:7]
	v_mfma_i32_16x16x64_i8 v[0:3], v[72:75], v[202:205], v[0:3]
	v_mfma_i32_16x16x64_i8 v[28:31], v[68:71], v[190:193], v[28:31]
	v_mfma_i32_16x16x64_i8 v[24:27], v[76:79], v[190:193], v[24:27]
	v_mfma_i32_16x16x64_i8 v[20:23], v[68:71], v[194:197], v[20:23]
	v_mfma_i32_16x16x64_i8 v[16:19], v[76:79], v[194:197], v[16:19]
	s_waitcnt lgkmcnt(1)
	v_mfma_i32_16x16x64_i8 v[12:15], v[68:71], v[206:209], v[12:15]
	v_mfma_i32_16x16x64_i8 v[8:11], v[76:79], v[206:209], v[8:11]
	s_waitcnt lgkmcnt(0)
	v_mfma_i32_16x16x64_i8 v[4:7], v[68:71], v[210:213], v[4:7]
	v_mfma_i32_16x16x64_i8 v[0:3], v[76:79], v[210:213], v[0:3]
	v_mfma_i32_16x16x64_i8 v[92:95], v[144:147], v[198:201], v[92:95]
	v_mfma_i32_16x16x64_i8 v[88:91], v[174:177], v[198:201], v[88:91]
	v_mfma_i32_16x16x64_i8 v[84:87], v[144:147], v[202:205], v[84:87]
	v_mfma_i32_16x16x64_i8 v[80:83], v[174:177], v[202:205], v[80:83]
	v_mfma_i32_16x16x64_i8 v[64:67], v[144:147], v[182:185], v[108:111]
	v_mfma_i32_16x16x64_i8 v[68:71], v[174:177], v[182:185], v[104:107]
	v_mfma_i32_16x16x64_i8 v[72:75], v[144:147], v[186:189], v[100:103]
	v_mfma_i32_16x16x64_i8 v[76:79], v[174:177], v[186:189], v[96:99]
	v_mfma_i32_16x16x64_i8 v[92:95], v[148:151], v[206:209], v[92:95]
	v_mfma_i32_16x16x64_i8 v[88:91], v[178:181], v[206:209], v[88:91]
	v_mfma_i32_16x16x64_i8 v[84:87], v[148:151], v[210:213], v[84:87]
	v_mfma_i32_16x16x64_i8 v[80:83], v[178:181], v[210:213], v[80:83]
	v_mfma_i32_16x16x64_i8 v[64:67], v[148:151], v[190:193], v[64:67]
	v_mfma_i32_16x16x64_i8 v[68:71], v[178:181], v[190:193], v[68:71]
	v_mfma_i32_16x16x64_i8 v[72:75], v[148:151], v[194:197], v[72:75]
	v_mfma_i32_16x16x64_i8 v[76:79], v[178:181], v[194:197], v[76:79]
	s_barrier
; #define PG8_STAGE(bufoff, gbase, voff) do { _Pragma("unroll") for (int _i = 0; _i < 2; ++_i) \
;         __builtin_amdgcn_raw_ptr_buffer_load_lds(rsrc, (LAS void*)(lds + (bufoff) + ldsw + _i * 8192), 16, (int)(voff)[_i], (int)(gbase), 0, 0); } while (0)
; #define PG8_STAGE_A(bufoff, h, goff) do { if constexpr (GATHER) { PG8_STAGE(bufoff, goff, vG[h]); } else { PG8_STAGE(bufoff, (goff) + (h) * hstep, voffA); } } while (0)
; #define PG8_WAIT_V(n) asm volatile("s_waitcnt vmcnt(" #n ")" ::: "memory")
; #define PG8_WAIT_L(n) asm volatile("s_waitcnt lgkmcnt(" #n ")" ::: "memory")
; #define PG8_BAR __builtin_amdgcn_s_barrier()
; #define PG8_SCHED __builtin_amdgcn_sched_barrier(0)
;     DI int row_cnt(const pg8::Unit& u) const { return __builtin_amdgcn_readfirstlane(tab[u.a0]) - u.ldc; }
;     ...
;             PG8_LDB(B0, 0, 0); PG8_LDB(B1, 0, 1); PG8_SCHED; PG8_LDA(At, 0, 0); PG8_STAGE_A(PG8_SA(1, 1), 1, a1);
;             if constexpr (GATHER) { if (last && has_next) load_rows((ui + 1) & 1, S.row_cnt(nxt)); }
;             PG8_WAIT_V(8); PG8_WAIT_L(0); PG8_BAR; PG8_MMA(0, 0, At, B0); PG8_MMA(0, 1, At, B1); PG8_BAR; PG8_SCHED;
;             PG8_LDA(At, 0, 1); PG8_STAGE(PG8_SB(0, 0), b2, voffB); PG8_STAGE(PG8_SB(0, 1), b2 + hstep, voffB); PG8_STAGE_A(PG8_SA(0, 0), 0, a2);
;             PG8_WAIT_V(8); PG8_WAIT_L(0); PG8_BAR; PG8_MMA(1, 0, At, B0); PG8_MMA(1, 1, At, B1); PG8_BAR; PG8_SCHED;
;             PG8_LDB(B0, 1, 0); PG8_LDB(B1, 1, 1); PG8_SCHED; PG8_LDA(At, 1, 0); PG8_STAGE_A(PG8_SA(0, 1), 1, a2);
;             PG8_WAIT_V(8); PG8_WAIT_L(0); PG8_BAR; PG8_MMA(0, 0, At, B0); PG8_MMA(0, 1, At, B1); PG8_BAR; PG8_SCHED;
;             PG8_LDA(At, 1, 1); PG8_STAGE(PG8_SB(1, 0), b3, voffB); PG8_STAGE(PG8_SB(1, 1), b3 + hstep, voffB); PG8_STAGE_A(PG8_SA(1, 0), 0, a3);
;             PG8_WAIT_V(8); PG8_WAIT_L(0); PG8_BAR; PG8_MMA(1, 0, At, B0); PG8_MMA(1, 1, At, B1); PG8_BAR; PG8_SCHED;
	s_add_i32 s54, 0, 0x18000
	v_add_u32_e32 v96, s54, v157
	v_add_u32_e32 v100, s54, v158
	s_add_i32 s54, 0, 0x1c000
	v_add_u32_e32 v144, s54, v157
	v_add_u32_e32 v148, s54, v158
	ds_read_b128 v[96:99], v96
	ds_read_b128 v[100:103], v100
	ds_read_b128 v[104:107], v169
	ds_read_b128 v[108:111], v170
	ds_read_b128 v[144:147], v144
	ds_read_b128 v[148:151], v148
	ds_read_b128 v[174:177], v171
	ds_read_b128 v[178:181], v172
	s_add_i32 s53, s53, 0x40000
	s_mov_b32 m0, s62
	ds_read_b128 v[182:185], v167 offset:32768
	ds_read_b128 v[186:189], v167 offset:34816
	ds_read_b128 v[190:193], v168 offset:32768
	ds_read_b128 v[194:197], v168 offset:34816
	ds_read_b128 v[198:201], v167 offset:36864
	ds_read_b128 v[202:205], v167 offset:38912
	ds_read_b128 v[206:209], v168 offset:36864
	ds_read_b128 v[210:213], v168 offset:38912
	buffer_load_dwordx4 v153, s[4:7], s53 offen lds
	s_mov_b32 m0, s63
	s_nop 0
	buffer_load_dwordx4 v155, s[4:7], s53 offen lds
	s_waitcnt vmcnt(8)
	s_waitcnt lgkmcnt(0)
	s_barrier
	s_waitcnt lgkmcnt(7)
	v_mfma_i32_16x16x64_i8 v[60:63], v[96:99], v[182:185], v[60:63]
	v_mfma_i32_16x16x64_i8 v[56:59], v[104:107], v[182:185], v[56:59]
	s_waitcnt lgkmcnt(6)
	v_mfma_i32_16x16x64_i8 v[52:55], v[96:99], v[186:189], v[52:55]
	v_mfma_i32_16x16x64_i8 v[48:51], v[104:107], v[186:189], v[48:51]
	s_waitcnt lgkmcnt(3)
	v_mfma_i32_16x16x64_i8 v[44:47], v[96:99], v[198:201], v[44:47]
	v_mfma_i32_16x16x64_i8 v[40:43], v[104:107], v[198:201], v[40:43]
	s_waitcnt lgkmcnt(2)
	v_mfma_i32_16x16x64_i8 v[36:39], v[96:99], v[202:205], v[36:39]
	v_mfma_i32_16x16x64_i8 v[32:35], v[104:107], v[202:205], v[32:35]
	v_mfma_i32_16x16x64_i8 v[60:63], v[100:103], v[190:193], v[60:63]
	v_mfma_i32_16x16x64_i8 v[56:59], v[108:111], v[190:193], v[56:59]
	v_mfma_i32_16x16x64_i8 v[52:55], v[100:103], v[194:197], v[52:55]
	v_mfma_i32_16x16x64_i8 v[48:51], v[108:111], v[194:197], v[48:51]
	s_waitcnt lgkmcnt(1)
	v_mfma_i32_16x16x64_i8 v[44:47], v[100:103], v[206:209], v[44:47]
	v_mfma_i32_16x16x64_i8 v[40:43], v[108:111], v[206:209], v[40:43]
	s_waitcnt lgkmcnt(0)
	v_mfma_i32_16x16x64_i8 v[36:39], v[100:103], v[210:213], v[36:39]
	v_mfma_i32_16x16x64_i8 v[32:35], v[108:111], v[210:213], v[32:35]
	v_mfma_i32_16x16x64_i8 v[140:143], v[144:147], v[182:185], v[140:143]
	v_mfma_i32_16x16x64_i8 v[136:139], v[174:177], v[182:185], v[136:139]
	v_mfma_i32_16x16x64_i8 v[132:135], v[144:147], v[186:189], v[132:135]
	v_mfma_i32_16x16x64_i8 v[128:131], v[174:177], v[186:189], v[128:131]
	v_mfma_i32_16x16x64_i8 v[124:127], v[144:147], v[198:201], v[124:127]
	v_mfma_i32_16x16x64_i8 v[120:123], v[174:177], v[198:201], v[120:123]
	v_mfma_i32_16x16x64_i8 v[116:119], v[144:147], v[202:205], v[116:119]
	v_mfma_i32_16x16x64_i8 v[112:115], v[174:177], v[202:205], v[112:115]
	v_mfma_i32_16x16x64_i8 v[140:143], v[148:151], v[190:193], v[140:143]
	v_mfma_i32_16x16x64_i8 v[136:139], v[178:181], v[190:193], v[136:139]
	v_mfma_i32_16x16x64_i8 v[132:135], v[148:151], v[194:197], v[132:135]
	v_mfma_i32_16x16x64_i8 v[128:131], v[178:181], v[194:197], v[128:131]
	v_mfma_i32_16x16x64_i8 v[124:127], v[148:151], v[206:209], v[124:127]
	v_mfma_i32_16x16x64_i8 v[120:123], v[178:181], v[206:209], v[120:123]
	v_mfma_i32_16x16x64_i8 v[116:119], v[148:151], v[210:213], v[116:119]
	v_mfma_i32_16x16x64_i8 v[112:115], v[178:181], v[210:213], v[112:115]
	s_barrier
	s_mov_b32 m0, s68
	s_add_i32 s53, s51, 0x80
	ds_read_b128 v[182:185], v167 offset:49152
	ds_read_b128 v[186:189], v167 offset:51200
	ds_read_b128 v[190:193], v168 offset:49152
	ds_read_b128 v[194:197], v168 offset:51200
	ds_read_b128 v[198:201], v167 offset:53248
	ds_read_b128 v[202:205], v167 offset:55296
	ds_read_b128 v[206:209], v168 offset:53248
	ds_read_b128 v[210:213], v168 offset:55296
	buffer_load_dwordx4 v154, s[4:7], s53 offen lds
	s_mov_b32 m0, s69
	s_add_i32 s51, s51, 0x40080
	buffer_load_dwordx4 v156, s[4:7], s53 offen lds
	s_mov_b32 m0, s72
	s_nop 0
	buffer_load_dwordx4 v154, s[4:7], s51 offen lds
	s_mov_b32 m0, s73
	s_nop 0
	buffer_load_dwordx4 v156, s[4:7], s51 offen lds
	s_mov_b32 m0, s70
	s_nop 0
	buffer_load_dwordx4 v153, s[4:7], s50 offen lds
	s_mov_b32 m0, s71
	s_nop 0
	buffer_load_dwordx4 v155, s[4:7], s50 offen lds
	s_waitcnt vmcnt(8)
	s_waitcnt lgkmcnt(0)
	s_barrier
	s_waitcnt lgkmcnt(7)
	v_mfma_i32_16x16x64_i8 v[28:31], v[96:99], v[182:185], v[28:31]
	v_mfma_i32_16x16x64_i8 v[24:27], v[104:107], v[182:185], v[24:27]
	s_waitcnt lgkmcnt(6)
	v_mfma_i32_16x16x64_i8 v[20:23], v[96:99], v[186:189], v[20:23]
	v_mfma_i32_16x16x64_i8 v[16:19], v[104:107], v[186:189], v[16:19]
	s_waitcnt lgkmcnt(3)
	v_mfma_i32_16x16x64_i8 v[12:15], v[96:99], v[198:201], v[12:15]
	v_mfma_i32_16x16x64_i8 v[8:11], v[104:107], v[198:201], v[8:11]
	s_waitcnt lgkmcnt(2)
	v_mfma_i32_16x16x64_i8 v[4:7], v[96:99], v[202:205], v[4:7]
	v_mfma_i32_16x16x64_i8 v[0:3], v[104:107], v[202:205], v[0:3]
	v_mfma_i32_16x16x64_i8 v[28:31], v[100:103], v[190:193], v[28:31]
	v_mfma_i32_16x16x64_i8 v[24:27], v[108:111], v[190:193], v[24:27]
	v_mfma_i32_16x16x64_i8 v[20:23], v[100:103], v[194:197], v[20:23]
	v_mfma_i32_16x16x64_i8 v[16:19], v[108:111], v[194:197], v[16:19]
	s_waitcnt lgkmcnt(1)
	v_mfma_i32_16x16x64_i8 v[12:15], v[100:103], v[206:209], v[12:15]
	v_mfma_i32_16x16x64_i8 v[8:11], v[108:111], v[206:209], v[8:11]
	s_waitcnt lgkmcnt(0)
	v_mfma_i32_16x16x64_i8 v[4:7], v[100:103], v[210:213], v[4:7]
	v_mfma_i32_16x16x64_i8 v[0:3], v[108:111], v[210:213], v[0:3]
	v_mfma_i32_16x16x64_i8 v[64:67], v[144:147], v[182:185], v[64:67]
	v_mfma_i32_16x16x64_i8 v[108:111], v[148:151], v[190:193], v[64:67]
	v_mfma_i32_16x16x64_i8 v[64:67], v[174:177], v[182:185], v[68:71]
	v_mfma_i32_16x16x64_i8 v[104:107], v[178:181], v[190:193], v[64:67]
	v_mfma_i32_16x16x64_i8 v[64:67], v[144:147], v[186:189], v[72:75]
	v_mfma_i32_16x16x64_i8 v[100:103], v[148:151], v[194:197], v[64:67]
	v_mfma_i32_16x16x64_i8 v[64:67], v[174:177], v[186:189], v[76:79]
	v_mfma_i32_16x16x64_i8 v[96:99], v[178:181], v[194:197], v[64:67]
	v_mfma_i32_16x16x64_i8 v[64:67], v[144:147], v[198:201], v[92:95]
	v_mfma_i32_16x16x64_i8 v[92:95], v[148:151], v[206:209], v[64:67]
	v_mfma_i32_16x16x64_i8 v[64:67], v[174:177], v[198:201], v[88:91]
	v_mfma_i32_16x16x64_i8 v[88:91], v[178:181], v[206:209], v[64:67]
	v_mfma_i32_16x16x64_i8 v[64:67], v[144:147], v[202:205], v[84:87]
	v_mfma_i32_16x16x64_i8 v[84:87], v[148:151], v[210:213], v[64:67]
	v_mfma_i32_16x16x64_i8 v[64:67], v[174:177], v[202:205], v[80:83]
	v_mfma_i32_16x16x64_i8 v[80:83], v[178:181], v[210:213], v[64:67]
	s_barrier
	s_add_i32 s10, s10, 2
	s_addk_i32 s2, 0x100
	s_addk_i32 s3, 0x100
	s_cmp_gt_u32 s10, 13
	s_cbranch_scc0 .LBB0_337
	s_and_b64 vcc, exec, s[12:13]
	s_cbranch_vccz .LBB0_340
	s_barrier

; #define PG8_STAGE(bufoff, gbase, voff) do { _Pragma("unroll") for (int _i = 0; _i < 2; ++_i) \
;         __builtin_amdgcn_raw_ptr_buffer_load_lds(rsrc, (LAS void*)(lds + (bufoff) + ldsw + _i * 8192), 16, (int)(voff)[_i], (int)(gbase), 0, 0); } while (0)
; #define PG8_STAGE_A(bufoff, h, goff) do { if constexpr (GATHER) { PG8_STAGE(bufoff, goff, vG[h]); } else { PG8_STAGE(bufoff, (goff) + (h) * hstep, voffA); } } while (0)
; #define PG8_WAIT_V(n) asm volatile("s_waitcnt vmcnt(" #n ")" ::: "memory")
; #define PG8_WAIT_L(n) asm volatile("s_waitcnt lgkmcnt(" #n ")" ::: "memory")
; #define PG8_BAR __builtin_amdgcn_s_barrier()
; #define PG8_SCHED __builtin_amdgcn_sched_barrier(0)
;     DI int row_cnt(const pg8::Unit& u) const { return __builtin_amdgcn_readfirstlane(tab[u.a0]) - u.ldc; }
;     ...
;             PG8_LDB(B0, 0, 0); PG8_LDB(B1, 0, 1); PG8_SCHED; PG8_LDA(At, 0, 0); PG8_STAGE_A(PG8_SA(1, 1), 1, a1);
;             if constexpr (GATHER) { if (last && has_next) load_rows((ui + 1) & 1, S.row_cnt(nxt)); }
;             PG8_WAIT_V(8); PG8_WAIT_L(0); PG8_BAR; PG8_MMA(0, 0, At, B0); PG8_MMA(0, 1, At, B1); PG8_BAR; PG8_SCHED;
;             PG8_LDA(At, 0, 1); PG8_STAGE(PG8_SB(0, 0), b2, voffB); PG8_STAGE(PG8_SB(0, 1), b2 + hstep, voffB); PG8_STAGE_A(PG8_SA(0, 0), 0, a2);
;             PG8_WAIT_V(8); PG8_WAIT_L(0); PG8_BAR; PG8_MMA(1, 0, At, B0); PG8_MMA(1, 1, At, B1); PG8_BAR; PG8_SCHED;
;             PG8_LDB(B0, 1, 0); PG8_LDB(B1, 1, 1); PG8_SCHED; PG8_LDA(At, 1, 0); PG8_STAGE_A(PG8_SA(0, 1), 1, a2);
;             PG8_WAIT_V(8); PG8_WAIT_L(0); PG8_BAR; PG8_MMA(0, 0, At, B0); PG8_MMA(0, 1, At, B1); PG8_BAR; PG8_SCHED;
;             PG8_LDA(At, 1, 1); PG8_STAGE(PG8_SB(1, 0), b3, voffB); PG8_STAGE(PG8_SB(1, 1), b3 + hstep, voffB); PG8_STAGE_A(PG8_SA(1, 0), 0, a3);
;             PG8_WAIT_V(8); PG8_WAIT_L(0); PG8_BAR; PG8_MMA(1, 0, At, B0); PG8_MMA(1, 1, At, B1); PG8_BAR; PG8_SCHED;
.LBB0_959:
	ds_read_b128 v[128:131], v140
	ds_read_b128 v[132:135], v141
	ds_read_b128 v[154:157], v142
	ds_read_b128 v[158:161], v143
	ds_read_b128 v[162:165], v144
	ds_read_b128 v[166:169], v145
	ds_read_b128 v[170:173], v146
	ds_read_b128 v[174:177], v147
	s_add_i32 s4, s2, 0xfffc0080
	s_cmp_eq_u32 s69, 12
	s_cselect_b32 s72, s65, s4
	s_cselect_b32 s71, s66, s3
	s_add_i32 s70, s72, 0x80
	s_mov_b32 s4, s74
	s_mov_b32 m0, s58
	ds_read_b128 v[178:181], v148
	ds_read_b128 v[182:185], v148 offset:2048
	ds_read_b128 v[186:189], v149
	ds_read_b128 v[190:193], v149 offset:2048
	ds_read_b128 v[194:197], v148 offset:4096
	ds_read_b128 v[198:201], v148 offset:6144
	ds_read_b128 v[202:205], v149 offset:4096
	ds_read_b128 v[206:209], v149 offset:6144
	buffer_load_dwordx4 v136, s[4:7], s2 offen lds
	s_mov_b32 m0, s61
	s_nop 0
	buffer_load_dwordx4 v137, s[4:7], s2 offen lds
	s_waitcnt vmcnt(8)
	s_waitcnt lgkmcnt(0)
	s_barrier
	s_waitcnt lgkmcnt(7)
	v_mfma_i32_16x16x64_i8 v[124:127], v[128:131], v[178:181], v[124:127]
	v_mfma_i32_16x16x64_i8 v[120:123], v[154:157], v[178:181], v[120:123]
	s_waitcnt lgkmcnt(6)
	v_mfma_i32_16x16x64_i8 v[108:111], v[128:131], v[182:185], v[108:111]
	v_mfma_i32_16x16x64_i8 v[104:107], v[154:157], v[182:185], v[104:107]
	s_waitcnt lgkmcnt(3)
	v_mfma_i32_16x16x64_i8 v[92:95], v[128:131], v[194:197], v[92:95]
	v_mfma_i32_16x16x64_i8 v[88:91], v[154:157], v[194:197], v[88:91]
	s_waitcnt lgkmcnt(2)
	v_mfma_i32_16x16x64_i8 v[76:79], v[128:131], v[198:201], v[76:79]
	v_mfma_i32_16x16x64_i8 v[72:75], v[154:157], v[198:201], v[72:75]
	v_mfma_i32_16x16x64_i8 v[124:127], v[132:135], v[186:189], v[124:127]
	v_mfma_i32_16x16x64_i8 v[120:123], v[158:161], v[186:189], v[120:123]
	v_mfma_i32_16x16x64_i8 v[108:111], v[132:135], v[190:193], v[108:111]
	v_mfma_i32_16x16x64_i8 v[104:107], v[158:161], v[190:193], v[104:107]
	s_waitcnt lgkmcnt(1)
	v_mfma_i32_16x16x64_i8 v[92:95], v[132:135], v[202:205], v[92:95]
	v_mfma_i32_16x16x64_i8 v[88:91], v[158:161], v[202:205], v[88:91]
	s_waitcnt lgkmcnt(0)
	v_mfma_i32_16x16x64_i8 v[76:79], v[132:135], v[206:209], v[76:79]
	v_mfma_i32_16x16x64_i8 v[72:75], v[158:161], v[206:209], v[72:75]
	v_mfma_i32_16x16x64_i8 v[116:119], v[162:165], v[178:181], v[116:119]
	v_mfma_i32_16x16x64_i8 v[112:115], v[170:173], v[178:181], v[112:115]
	v_mfma_i32_16x16x64_i8 v[100:103], v[162:165], v[182:185], v[100:103]
	v_mfma_i32_16x16x64_i8 v[96:99], v[170:173], v[182:185], v[96:99]
	v_mfma_i32_16x16x64_i8 v[84:87], v[162:165], v[194:197], v[84:87]
	v_mfma_i32_16x16x64_i8 v[80:83], v[170:173], v[194:197], v[80:83]
	v_mfma_i32_16x16x64_i8 v[68:71], v[162:165], v[198:201], v[68:71]
	v_mfma_i32_16x16x64_i8 v[64:67], v[170:173], v[198:201], v[64:67]
	v_mfma_i32_16x16x64_i8 v[116:119], v[166:169], v[186:189], v[116:119]
	v_mfma_i32_16x16x64_i8 v[112:115], v[174:177], v[186:189], v[112:115]
	v_mfma_i32_16x16x64_i8 v[100:103], v[166:169], v[190:193], v[100:103]
	v_mfma_i32_16x16x64_i8 v[96:99], v[174:177], v[190:193], v[96:99]
	v_mfma_i32_16x16x64_i8 v[84:87], v[166:169], v[202:205], v[84:87]
	v_mfma_i32_16x16x64_i8 v[80:83], v[174:177], v[202:205], v[80:83]
	v_mfma_i32_16x16x64_i8 v[68:71], v[166:169], v[206:209], v[68:71]
	v_mfma_i32_16x16x64_i8 v[64:67], v[174:177], v[206:209], v[64:67]
	s_barrier
	s_mov_b32 m0, s1
	ds_read_b128 v[178:181], v148 offset:16384
	ds_read_b128 v[182:185], v148 offset:18432
	ds_read_b128 v[186:189], v149 offset:16384
	ds_read_b128 v[190:193], v149 offset:18432
	ds_read_b128 v[194:197], v148 offset:20480
	ds_read_b128 v[198:201], v148 offset:22528
	ds_read_b128 v[202:205], v149 offset:20480
	ds_read_b128 v[206:209], v149 offset:22528
	buffer_load_dwordx4 v136, s[4:7], s71 offen lds
	s_mov_b32 m0, s33
	s_add_i32 s73, s71, 0x40000
	buffer_load_dwordx4 v137, s[4:7], s71 offen lds
	s_mov_b32 m0, s34
	s_nop 0
	buffer_load_dwordx4 v136, s[4:7], s73 offen lds
	s_mov_b32 m0, s35
	s_nop 0
	buffer_load_dwordx4 v137, s[4:7], s73 offen lds
	s_mov_b32 m0, s0
	s_nop 0
	buffer_load_dwordx4 v136, s[4:7], s72 offen lds
	s_mov_b32 m0, s48
	s_nop 0
	buffer_load_dwordx4 v137, s[4:7], s72 offen lds
	s_waitcnt vmcnt(8)
	s_waitcnt lgkmcnt(0)
	s_barrier
	s_waitcnt lgkmcnt(7)
	v_mfma_i32_16x16x64_i8 v[60:63], v[128:131], v[178:181], v[60:63]
	v_mfma_i32_16x16x64_i8 v[56:59], v[154:157], v[178:181], v[56:59]
	s_waitcnt lgkmcnt(6)
	v_mfma_i32_16x16x64_i8 v[44:47], v[128:131], v[182:185], v[44:47]
	v_mfma_i32_16x16x64_i8 v[40:43], v[154:157], v[182:185], v[40:43]
	s_waitcnt lgkmcnt(3)
	v_mfma_i32_16x16x64_i8 v[28:31], v[128:131], v[194:197], v[28:31]
	v_mfma_i32_16x16x64_i8 v[24:27], v[154:157], v[194:197], v[24:27]
	s_waitcnt lgkmcnt(2)
	v_mfma_i32_16x16x64_i8 v[12:15], v[128:131], v[198:201], v[12:15]
	v_mfma_i32_16x16x64_i8 v[8:11], v[154:157], v[198:201], v[8:11]
	v_mfma_i32_16x16x64_i8 v[60:63], v[132:135], v[186:189], v[60:63]
	v_mfma_i32_16x16x64_i8 v[56:59], v[158:161], v[186:189], v[56:59]
	v_mfma_i32_16x16x64_i8 v[44:47], v[132:135], v[190:193], v[44:47]
	v_mfma_i32_16x16x64_i8 v[40:43], v[158:161], v[190:193], v[40:43]
	s_waitcnt lgkmcnt(1)
	v_mfma_i32_16x16x64_i8 v[28:31], v[132:135], v[202:205], v[28:31]
	v_mfma_i32_16x16x64_i8 v[24:27], v[158:161], v[202:205], v[24:27]
	s_waitcnt lgkmcnt(0)
	v_mfma_i32_16x16x64_i8 v[12:15], v[132:135], v[206:209], v[12:15]
	v_mfma_i32_16x16x64_i8 v[8:11], v[158:161], v[206:209], v[8:11]
	v_mfma_i32_16x16x64_i8 v[52:55], v[162:165], v[178:181], v[52:55]
	v_mfma_i32_16x16x64_i8 v[48:51], v[170:173], v[178:181], v[48:51]
	v_mfma_i32_16x16x64_i8 v[36:39], v[162:165], v[182:185], v[36:39]
	v_mfma_i32_16x16x64_i8 v[32:35], v[170:173], v[182:185], v[32:35]
	v_mfma_i32_16x16x64_i8 v[20:23], v[162:165], v[194:197], v[20:23]
	v_mfma_i32_16x16x64_i8 v[16:19], v[170:173], v[194:197], v[16:19]
	v_mfma_i32_16x16x64_i8 v[4:7], v[162:165], v[198:201], v[4:7]
	v_mfma_i32_16x16x64_i8 v[0:3], v[170:173], v[198:201], v[0:3]
	v_mfma_i32_16x16x64_i8 v[52:55], v[166:169], v[186:189], v[52:55]
	v_mfma_i32_16x16x64_i8 v[48:51], v[174:177], v[186:189], v[48:51]
	v_mfma_i32_16x16x64_i8 v[36:39], v[166:169], v[190:193], v[36:39]
	v_mfma_i32_16x16x64_i8 v[32:35], v[174:177], v[190:193], v[32:35]
	v_mfma_i32_16x16x64_i8 v[20:23], v[166:169], v[202:205], v[20:23]
	v_mfma_i32_16x16x64_i8 v[16:19], v[174:177], v[202:205], v[16:19]
	v_mfma_i32_16x16x64_i8 v[4:7], v[166:169], v[206:209], v[4:7]
	v_mfma_i32_16x16x64_i8 v[0:3], v[174:177], v[206:209], v[0:3]
	s_barrier
; #define PG8_STAGE(bufoff, gbase, voff) do { _Pragma("unroll") for (int _i = 0; _i < 2; ++_i) \
;         __builtin_amdgcn_raw_ptr_buffer_load_lds(rsrc, (LAS void*)(lds + (bufoff) + ldsw + _i * 8192), 16, (int)(voff)[_i], (int)(gbase), 0, 0); } while (0)
; #define PG8_STAGE_A(bufoff, h, goff) do { if constexpr (GATHER) { PG8_STAGE(bufoff, goff, vG[h]); } else { PG8_STAGE(bufoff, (goff) + (h) * hstep, voffA); } } while (0)
; #define PG8_WAIT_V(n) asm volatile("s_waitcnt vmcnt(" #n ")" ::: "memory")
; #define PG8_WAIT_L(n) asm volatile("s_waitcnt lgkmcnt(" #n ")" ::: "memory")
; #define PG8_BAR __builtin_amdgcn_s_barrier()
; #define PG8_SCHED __builtin_amdgcn_sched_barrier(0)
;     DI int row_cnt(const pg8::Unit& u) const { return __builtin_amdgcn_readfirstlane(tab[u.a0]) - u.ldc; }
;     ...
;             PG8_LDB(B0, 0, 0); PG8_LDB(B1, 0, 1); PG8_SCHED; PG8_LDA(At, 0, 0); PG8_STAGE_A(PG8_SA(1, 1), 1, a1);
;             if constexpr (GATHER) { if (last && has_next) load_rows((ui + 1) & 1, S.row_cnt(nxt)); }
;             PG8_WAIT_V(8); PG8_WAIT_L(0); PG8_BAR; PG8_MMA(0, 0, At, B0); PG8_MMA(0, 1, At, B1); PG8_BAR; PG8_SCHED;
;             PG8_LDA(At, 0, 1); PG8_STAGE(PG8_SB(0, 0), b2, voffB); PG8_STAGE(PG8_SB(0, 1), b2 + hstep, voffB); PG8_STAGE_A(PG8_SA(0, 0), 0, a2);
;             PG8_WAIT_V(8); PG8_WAIT_L(0); PG8_BAR; PG8_MMA(1, 0, At, B0); PG8_MMA(1, 1, At, B1); PG8_BAR; PG8_SCHED;
;             PG8_LDB(B0, 1, 0); PG8_LDB(B1, 1, 1); PG8_SCHED; PG8_LDA(At, 1, 0); PG8_STAGE_A(PG8_SA(0, 1), 1, a2);
;             PG8_WAIT_V(8); PG8_WAIT_L(0); PG8_BAR; PG8_MMA(0, 0, At, B0); PG8_MMA(0, 1, At, B1); PG8_BAR; PG8_SCHED;
;             PG8_LDA(At, 1, 1); PG8_STAGE(PG8_SB(1, 0), b3, voffB); PG8_STAGE(PG8_SB(1, 1), b3 + hstep, voffB); PG8_STAGE_A(PG8_SA(1, 0), 0, a3);
;             PG8_WAIT_V(8); PG8_WAIT_L(0); PG8_BAR; PG8_MMA(1, 0, At, B0); PG8_MMA(1, 1, At, B1); PG8_BAR; PG8_SCHED;
	s_add_i32 s73, 0, 0x18000
	v_add_u32_e32 v128, s73, v138
	v_add_u32_e32 v132, s73, v139
	s_add_i32 s73, 0, 0x1c000
	v_add_u32_e32 v162, s73, v138
	v_add_u32_e32 v166, s73, v139
	ds_read_b128 v[128:131], v128
	ds_read_b128 v[132:135], v132
	ds_read_b128 v[154:157], v150
	ds_read_b128 v[158:161], v151
	ds_read_b128 v[162:165], v162
	ds_read_b128 v[166:169], v166
	ds_read_b128 v[170:173], v152
	ds_read_b128 v[174:177], v153
	s_add_i32 s72, s72, 0x40000
	s_mov_b32 m0, s49
	ds_read_b128 v[178:181], v148 offset:32768
	ds_read_b128 v[182:185], v148 offset:34816
	ds_read_b128 v[186:189], v149 offset:32768
	ds_read_b128 v[190:193], v149 offset:34816
	ds_read_b128 v[194:197], v148 offset:36864
	ds_read_b128 v[198:201], v148 offset:38912
	ds_read_b128 v[202:205], v149 offset:36864
	ds_read_b128 v[206:209], v149 offset:38912
	buffer_load_dwordx4 v136, s[4:7], s72 offen lds
	s_mov_b32 m0, s50
	s_nop 0
	buffer_load_dwordx4 v137, s[4:7], s72 offen lds
	s_waitcnt vmcnt(8)
	s_waitcnt lgkmcnt(0)
	s_barrier
	s_waitcnt lgkmcnt(7)
	v_mfma_i32_16x16x64_i8 v[124:127], v[128:131], v[178:181], v[124:127]
	v_mfma_i32_16x16x64_i8 v[120:123], v[154:157], v[178:181], v[120:123]
	s_waitcnt lgkmcnt(6)
	v_mfma_i32_16x16x64_i8 v[108:111], v[128:131], v[182:185], v[108:111]
	v_mfma_i32_16x16x64_i8 v[104:107], v[154:157], v[182:185], v[104:107]
	s_waitcnt lgkmcnt(3)
	v_mfma_i32_16x16x64_i8 v[92:95], v[128:131], v[194:197], v[92:95]
	v_mfma_i32_16x16x64_i8 v[88:91], v[154:157], v[194:197], v[88:91]
	s_waitcnt lgkmcnt(2)
	v_mfma_i32_16x16x64_i8 v[76:79], v[128:131], v[198:201], v[76:79]
	v_mfma_i32_16x16x64_i8 v[72:75], v[154:157], v[198:201], v[72:75]
	v_mfma_i32_16x16x64_i8 v[124:127], v[132:135], v[186:189], v[124:127]
	v_mfma_i32_16x16x64_i8 v[120:123], v[158:161], v[186:189], v[120:123]
	v_mfma_i32_16x16x64_i8 v[108:111], v[132:135], v[190:193], v[108:111]
	v_mfma_i32_16x16x64_i8 v[104:107], v[158:161], v[190:193], v[104:107]
	s_waitcnt lgkmcnt(1)
	v_mfma_i32_16x16x64_i8 v[92:95], v[132:135], v[202:205], v[92:95]
	v_mfma_i32_16x16x64_i8 v[88:91], v[158:161], v[202:205], v[88:91]
	s_waitcnt lgkmcnt(0)
	v_mfma_i32_16x16x64_i8 v[76:79], v[132:135], v[206:209], v[76:79]
	v_mfma_i32_16x16x64_i8 v[72:75], v[158:161], v[206:209], v[72:75]
	v_mfma_i32_16x16x64_i8 v[116:119], v[162:165], v[178:181], v[116:119]
	v_mfma_i32_16x16x64_i8 v[112:115], v[170:173], v[178:181], v[112:115]
	v_mfma_i32_16x16x64_i8 v[100:103], v[162:165], v[182:185], v[100:103]
	v_mfma_i32_16x16x64_i8 v[96:99], v[170:173], v[182:185], v[96:99]
	v_mfma_i32_16x16x64_i8 v[84:87], v[162:165], v[194:197], v[84:87]
	v_mfma_i32_16x16x64_i8 v[80:83], v[170:173], v[194:197], v[80:83]
	v_mfma_i32_16x16x64_i8 v[68:71], v[162:165], v[198:201], v[68:71]
	v_mfma_i32_16x16x64_i8 v[64:67], v[170:173], v[198:201], v[64:67]
	v_mfma_i32_16x16x64_i8 v[116:119], v[166:169], v[186:189], v[116:119]
	v_mfma_i32_16x16x64_i8 v[112:115], v[174:177], v[186:189], v[112:115]
	v_mfma_i32_16x16x64_i8 v[100:103], v[166:169], v[190:193], v[100:103]
	v_mfma_i32_16x16x64_i8 v[96:99], v[174:177], v[190:193], v[96:99]
	v_mfma_i32_16x16x64_i8 v[84:87], v[166:169], v[202:205], v[84:87]
	v_mfma_i32_16x16x64_i8 v[80:83], v[174:177], v[202:205], v[80:83]
	v_mfma_i32_16x16x64_i8 v[68:71], v[166:169], v[206:209], v[68:71]
	v_mfma_i32_16x16x64_i8 v[64:67], v[174:177], v[206:209], v[64:67]
	s_barrier
	s_mov_b32 m0, s52
	s_add_i32 s72, s71, 0x80
	ds_read_b128 v[178:181], v148 offset:49152
	ds_read_b128 v[182:185], v148 offset:51200
	ds_read_b128 v[186:189], v149 offset:49152
	ds_read_b128 v[190:193], v149 offset:51200
	ds_read_b128 v[194:197], v148 offset:53248
	ds_read_b128 v[198:201], v148 offset:55296
	ds_read_b128 v[202:205], v149 offset:53248
	ds_read_b128 v[206:209], v149 offset:55296
	buffer_load_dwordx4 v136, s[4:7], s72 offen lds
	s_mov_b32 m0, s53
	s_add_i32 s71, s71, 0x40080
	buffer_load_dwordx4 v137, s[4:7], s72 offen lds
	s_mov_b32 m0, s56
	s_nop 0
	buffer_load_dwordx4 v136, s[4:7], s71 offen lds
	s_mov_b32 m0, s57
	s_nop 0
	buffer_load_dwordx4 v137, s[4:7], s71 offen lds
	s_mov_b32 m0, s54
	s_nop 0
	buffer_load_dwordx4 v136, s[4:7], s70 offen lds
	s_mov_b32 m0, s55
	s_nop 0
	buffer_load_dwordx4 v137, s[4:7], s70 offen lds
	s_waitcnt vmcnt(8)
	s_waitcnt lgkmcnt(0)
	s_barrier
	s_waitcnt lgkmcnt(7)
	v_mfma_i32_16x16x64_i8 v[60:63], v[128:131], v[178:181], v[60:63]
	v_mfma_i32_16x16x64_i8 v[56:59], v[154:157], v[178:181], v[56:59]
	s_waitcnt lgkmcnt(6)
	v_mfma_i32_16x16x64_i8 v[44:47], v[128:131], v[182:185], v[44:47]
	v_mfma_i32_16x16x64_i8 v[40:43], v[154:157], v[182:185], v[40:43]
	s_waitcnt lgkmcnt(3)
	v_mfma_i32_16x16x64_i8 v[28:31], v[128:131], v[194:197], v[28:31]
	v_mfma_i32_16x16x64_i8 v[24:27], v[154:157], v[194:197], v[24:27]
	s_waitcnt lgkmcnt(2)
	v_mfma_i32_16x16x64_i8 v[12:15], v[128:131], v[198:201], v[12:15]
	v_mfma_i32_16x16x64_i8 v[8:11], v[154:157], v[198:201], v[8:11]
	v_mfma_i32_16x16x64_i8 v[60:63], v[132:135], v[186:189], v[60:63]
	v_mfma_i32_16x16x64_i8 v[56:59], v[158:161], v[186:189], v[56:59]
	v_mfma_i32_16x16x64_i8 v[44:47], v[132:135], v[190:193], v[44:47]
	v_mfma_i32_16x16x64_i8 v[40:43], v[158:161], v[190:193], v[40:43]
	s_waitcnt lgkmcnt(1)
	v_mfma_i32_16x16x64_i8 v[28:31], v[132:135], v[202:205], v[28:31]
	v_mfma_i32_16x16x64_i8 v[24:27], v[158:161], v[202:205], v[24:27]
	s_waitcnt lgkmcnt(0)
	v_mfma_i32_16x16x64_i8 v[12:15], v[132:135], v[206:209], v[12:15]
	v_mfma_i32_16x16x64_i8 v[8:11], v[158:161], v[206:209], v[8:11]
	v_mfma_i32_16x16x64_i8 v[52:55], v[162:165], v[178:181], v[52:55]
	v_mfma_i32_16x16x64_i8 v[48:51], v[170:173], v[178:181], v[48:51]
	v_mfma_i32_16x16x64_i8 v[36:39], v[162:165], v[182:185], v[36:39]
	v_mfma_i32_16x16x64_i8 v[32:35], v[170:173], v[182:185], v[32:35]
	v_mfma_i32_16x16x64_i8 v[20:23], v[162:165], v[194:197], v[20:23]
	v_mfma_i32_16x16x64_i8 v[16:19], v[170:173], v[194:197], v[16:19]
	v_mfma_i32_16x16x64_i8 v[4:7], v[162:165], v[198:201], v[4:7]
	v_mfma_i32_16x16x64_i8 v[0:3], v[170:173], v[198:201], v[0:3]
	v_mfma_i32_16x16x64_i8 v[52:55], v[166:169], v[186:189], v[52:55]
	v_mfma_i32_16x16x64_i8 v[48:51], v[174:177], v[186:189], v[48:51]
	v_mfma_i32_16x16x64_i8 v[36:39], v[166:169], v[190:193], v[36:39]
	v_mfma_i32_16x16x64_i8 v[32:35], v[174:177], v[190:193], v[32:35]
	v_mfma_i32_16x16x64_i8 v[20:23], v[166:169], v[202:205], v[20:23]
	v_mfma_i32_16x16x64_i8 v[16:19], v[174:177], v[202:205], v[16:19]
	v_mfma_i32_16x16x64_i8 v[4:7], v[166:169], v[206:209], v[4:7]
	v_mfma_i32_16x16x64_i8 v[0:3], v[174:177], v[206:209], v[0:3]
	s_barrier
	s_add_i32 s69, s69, 2
	s_addk_i32 s2, 0x100
	s_addk_i32 s3, 0x100
	s_cmp_gt_u32 s69, 13
	s_cbranch_scc0 .LBB0_959
	s_and_b64 vcc, exec, s[18:19]
	s_cbranch_vccz .LBB0_962
	s_barrier

; #define PG8_STAGE(bufoff, gbase, voff) do { _Pragma("unroll") for (int _i = 0; _i < 2; ++_i) \
;         __builtin_amdgcn_raw_ptr_buffer_load_lds(rsrc, (LAS void*)(lds + (bufoff) + ldsw + _i * 8192), 16, (int)(voff)[_i], (int)(gbase), 0, 0); } while (0)
; #define PG8_STAGE_A(bufoff, h, goff) do { if constexpr (GATHER) { PG8_STAGE(bufoff, goff, vG[h]); } else { PG8_STAGE(bufoff, (goff) + (h) * hstep, voffA); } } while (0)
; #define PG8_WAIT_V(n) asm volatile("s_waitcnt vmcnt(" #n ")" ::: "memory")
; #define PG8_WAIT_L(n) asm volatile("s_waitcnt lgkmcnt(" #n ")" ::: "memory")
; #define PG8_BAR __builtin_amdgcn_s_barrier()
; #define PG8_SCHED __builtin_amdgcn_sched_barrier(0)
;     DI int row_cnt(const pg8::Unit& u) const { return __builtin_amdgcn_readfirstlane(tab[u.a0]) - u.ldc; }
;     ...
;             PG8_LDB(B0, 0, 0); PG8_LDB(B1, 0, 1); PG8_SCHED; PG8_LDA(At, 0, 0); PG8_STAGE_A(PG8_SA(1, 1), 1, a1);
;             if constexpr (GATHER) { if (last && has_next) load_rows((ui + 1) & 1, S.row_cnt(nxt)); }
;             PG8_WAIT_V(8); PG8_WAIT_L(0); PG8_BAR; PG8_MMA(0, 0, At, B0); PG8_MMA(0, 1, At, B1); PG8_BAR; PG8_SCHED;
;             PG8_LDA(At, 0, 1); PG8_STAGE(PG8_SB(0, 0), b2, voffB); PG8_STAGE(PG8_SB(0, 1), b2 + hstep, voffB); PG8_STAGE_A(PG8_SA(0, 0), 0, a2);
;             PG8_WAIT_V(8); PG8_WAIT_L(0); PG8_BAR; PG8_MMA(1, 0, At, B0); PG8_MMA(1, 1, At, B1); PG8_BAR; PG8_SCHED;
;             PG8_LDB(B0, 1, 0); PG8_LDB(B1, 1, 1); PG8_SCHED; PG8_LDA(At, 1, 0); PG8_STAGE_A(PG8_SA(0, 1), 1, a2);
;             PG8_WAIT_V(8); PG8_WAIT_L(0); PG8_BAR; PG8_MMA(0, 0, At, B0); PG8_MMA(0, 1, At, B1); PG8_BAR; PG8_SCHED;
;             PG8_LDA(At, 1, 1); PG8_STAGE(PG8_SB(1, 0), b3, voffB); PG8_STAGE(PG8_SB(1, 1), b3 + hstep, voffB); PG8_STAGE_A(PG8_SA(1, 0), 0, a3);
;             PG8_WAIT_V(8); PG8_WAIT_L(0); PG8_BAR; PG8_MMA(1, 0, At, B0); PG8_MMA(1, 1, At, B1); PG8_BAR; PG8_SCHED;
.LBB0_1102:
	ds_read_b128 v[64:67], v82
	ds_read_b128 v[68:71], v83
	ds_read_b128 v[72:75], v84
	ds_read_b128 v[90:93], v85
	s_add_i32 s4, s2, 0xfff80080
	s_cmp_eq_u32 s52, 28
	s_cselect_b32 s53, s48, s4
	s_cselect_b32 s54, s49, s3
	s_add_i32 s55, s53, 0x80
	s_mov_b32 s4, s58
	s_mov_b32 m0, s45
	ds_read_b128 v[94:97], v86
	ds_read_b128 v[98:101], v86 offset:2048
	ds_read_b128 v[102:105], v87
	ds_read_b128 v[106:109], v87 offset:2048
	ds_read_b128 v[110:113], v86 offset:4096
	ds_read_b128 v[114:117], v86 offset:6144
	ds_read_b128 v[118:121], v87 offset:4096
	ds_read_b128 v[122:125], v87 offset:6144
	buffer_load_dwordx4 v76, s[4:7], s2 offen lds
	s_mov_b32 m0, s47
	s_nop 0
	buffer_load_dwordx4 v78, s[4:7], s2 offen lds
	s_waitcnt vmcnt(8)
	s_waitcnt lgkmcnt(0)
	s_barrier
	s_waitcnt lgkmcnt(7)
	v_mfma_f32_16x16x32_bf16 v[60:63], v[64:67], v[94:97], v[60:63]
	v_mfma_f32_16x16x32_bf16 v[56:59], v[72:75], v[94:97], v[56:59]
	s_waitcnt lgkmcnt(6)
	v_mfma_f32_16x16x32_bf16 v[52:55], v[64:67], v[98:101], v[52:55]
	v_mfma_f32_16x16x32_bf16 v[48:51], v[72:75], v[98:101], v[48:51]
	s_waitcnt lgkmcnt(3)
	v_mfma_f32_16x16x32_bf16 v[44:47], v[64:67], v[110:113], v[44:47]
	v_mfma_f32_16x16x32_bf16 v[40:43], v[72:75], v[110:113], v[40:43]
	s_waitcnt lgkmcnt(2)
	v_mfma_f32_16x16x32_bf16 v[36:39], v[64:67], v[114:117], v[36:39]
	v_mfma_f32_16x16x32_bf16 v[32:35], v[72:75], v[114:117], v[32:35]
	v_mfma_f32_16x16x32_bf16 v[60:63], v[68:71], v[102:105], v[60:63]
	v_mfma_f32_16x16x32_bf16 v[56:59], v[90:93], v[102:105], v[56:59]
	v_mfma_f32_16x16x32_bf16 v[52:55], v[68:71], v[106:109], v[52:55]
	v_mfma_f32_16x16x32_bf16 v[48:51], v[90:93], v[106:109], v[48:51]
	s_waitcnt lgkmcnt(1)
	v_mfma_f32_16x16x32_bf16 v[44:47], v[68:71], v[118:121], v[44:47]
	v_mfma_f32_16x16x32_bf16 v[40:43], v[90:93], v[118:121], v[40:43]
	s_waitcnt lgkmcnt(0)
	v_mfma_f32_16x16x32_bf16 v[36:39], v[68:71], v[122:125], v[36:39]
	v_mfma_f32_16x16x32_bf16 v[32:35], v[90:93], v[122:125], v[32:35]
	s_barrier
	s_mov_b32 m0, s24
	ds_read_b128 v[94:97], v86 offset:16384
	ds_read_b128 v[98:101], v86 offset:18432
	ds_read_b128 v[102:105], v87 offset:16384
	ds_read_b128 v[106:109], v87 offset:18432
	ds_read_b128 v[110:113], v86 offset:20480
	ds_read_b128 v[114:117], v86 offset:22528
	ds_read_b128 v[118:121], v87 offset:20480
	ds_read_b128 v[122:125], v87 offset:22528
	buffer_load_dwordx4 v77, s[4:7], s54 offen lds
	s_mov_b32 m0, s25
	s_add_i32 s56, s54, 0x80000
	buffer_load_dwordx4 v79, s[4:7], s54 offen lds
	s_mov_b32 m0, s26
	s_nop 0
	buffer_load_dwordx4 v77, s[4:7], s56 offen lds
	s_mov_b32 m0, s27
	s_nop 0
	buffer_load_dwordx4 v79, s[4:7], s56 offen lds
	s_mov_b32 m0, s23
	s_nop 0
	buffer_load_dwordx4 v76, s[4:7], s53 offen lds
	s_mov_b32 m0, s33
	s_nop 0
	buffer_load_dwordx4 v78, s[4:7], s53 offen lds
	s_waitcnt vmcnt(8)
	s_waitcnt lgkmcnt(0)
	s_barrier
	s_waitcnt lgkmcnt(7)
	v_mfma_f32_16x16x32_bf16 v[28:31], v[64:67], v[94:97], v[28:31]
	v_mfma_f32_16x16x32_bf16 v[24:27], v[72:75], v[94:97], v[24:27]
	s_waitcnt lgkmcnt(6)
	v_mfma_f32_16x16x32_bf16 v[20:23], v[64:67], v[98:101], v[20:23]
	v_mfma_f32_16x16x32_bf16 v[16:19], v[72:75], v[98:101], v[16:19]
	s_waitcnt lgkmcnt(3)
	v_mfma_f32_16x16x32_bf16 v[12:15], v[64:67], v[110:113], v[12:15]
	v_mfma_f32_16x16x32_bf16 v[8:11], v[72:75], v[110:113], v[8:11]
	s_waitcnt lgkmcnt(2)
	v_mfma_f32_16x16x32_bf16 v[4:7], v[64:67], v[114:117], v[4:7]
	v_mfma_f32_16x16x32_bf16 v[0:3], v[72:75], v[114:117], v[0:3]
	v_mfma_f32_16x16x32_bf16 v[28:31], v[68:71], v[102:105], v[28:31]
	v_mfma_f32_16x16x32_bf16 v[24:27], v[90:93], v[102:105], v[24:27]
	v_mfma_f32_16x16x32_bf16 v[20:23], v[68:71], v[106:109], v[20:23]
	v_mfma_f32_16x16x32_bf16 v[16:19], v[90:93], v[106:109], v[16:19]
	s_waitcnt lgkmcnt(1)
	v_mfma_f32_16x16x32_bf16 v[12:15], v[68:71], v[118:121], v[12:15]
	v_mfma_f32_16x16x32_bf16 v[8:11], v[90:93], v[118:121], v[8:11]
	s_waitcnt lgkmcnt(0)
	v_mfma_f32_16x16x32_bf16 v[4:7], v[68:71], v[122:125], v[4:7]
	v_mfma_f32_16x16x32_bf16 v[0:3], v[90:93], v[122:125], v[0:3]
	s_barrier
; #define PG8_STAGE(bufoff, gbase, voff) do { _Pragma("unroll") for (int _i = 0; _i < 2; ++_i) \
;         __builtin_amdgcn_raw_ptr_buffer_load_lds(rsrc, (LAS void*)(lds + (bufoff) + ldsw + _i * 8192), 16, (int)(voff)[_i], (int)(gbase), 0, 0); } while (0)
; #define PG8_STAGE_A(bufoff, h, goff) do { if constexpr (GATHER) { PG8_STAGE(bufoff, goff, vG[h]); } else { PG8_STAGE(bufoff, (goff) + (h) * hstep, voffA); } } while (0)
; #define PG8_WAIT_V(n) asm volatile("s_waitcnt vmcnt(" #n ")" ::: "memory")
; #define PG8_WAIT_L(n) asm volatile("s_waitcnt lgkmcnt(" #n ")" ::: "memory")
; #define PG8_BAR __builtin_amdgcn_s_barrier()
; #define PG8_SCHED __builtin_amdgcn_sched_barrier(0)
;     DI int row_cnt(const pg8::Unit& u) const { return __builtin_amdgcn_readfirstlane(tab[u.a0]) - u.ldc; }
;     ...
;             PG8_LDB(B0, 0, 0); PG8_LDB(B1, 0, 1); PG8_SCHED; PG8_LDA(At, 0, 0); PG8_STAGE_A(PG8_SA(1, 1), 1, a1);
;             if constexpr (GATHER) { if (last && has_next) load_rows((ui + 1) & 1, S.row_cnt(nxt)); }
;             PG8_WAIT_V(8); PG8_WAIT_L(0); PG8_BAR; PG8_MMA(0, 0, At, B0); PG8_MMA(0, 1, At, B1); PG8_BAR; PG8_SCHED;
;             PG8_LDA(At, 0, 1); PG8_STAGE(PG8_SB(0, 0), b2, voffB); PG8_STAGE(PG8_SB(0, 1), b2 + hstep, voffB); PG8_STAGE_A(PG8_SA(0, 0), 0, a2);
;             PG8_WAIT_V(8); PG8_WAIT_L(0); PG8_BAR; PG8_MMA(1, 0, At, B0); PG8_MMA(1, 1, At, B1); PG8_BAR; PG8_SCHED;
;             PG8_LDB(B0, 1, 0); PG8_LDB(B1, 1, 1); PG8_SCHED; PG8_LDA(At, 1, 0); PG8_STAGE_A(PG8_SA(0, 1), 1, a2);
;             PG8_WAIT_V(8); PG8_WAIT_L(0); PG8_BAR; PG8_MMA(0, 0, At, B0); PG8_MMA(0, 1, At, B1); PG8_BAR; PG8_SCHED;
;             PG8_LDA(At, 1, 1); PG8_STAGE(PG8_SB(1, 0), b3, voffB); PG8_STAGE(PG8_SB(1, 1), b3 + hstep, voffB); PG8_STAGE_A(PG8_SA(1, 0), 0, a3);
;             PG8_WAIT_V(8); PG8_WAIT_L(0); PG8_BAR; PG8_MMA(1, 0, At, B0); PG8_MMA(1, 1, At, B1); PG8_BAR; PG8_SCHED;
	s_add_i32 s56, 0, 0x18000
	v_add_u32_e32 v64, s56, v80
	v_add_u32_e32 v68, s56, v81
	ds_read_b128 v[64:67], v64
	ds_read_b128 v[68:71], v68
	ds_read_b128 v[72:75], v88
	ds_read_b128 v[90:93], v89
	s_add_i32 s53, s53, 0x80000
	s_mov_b32 m0, s34
	ds_read_b128 v[94:97], v86 offset:32768
	ds_read_b128 v[98:101], v86 offset:34816
	ds_read_b128 v[102:105], v87 offset:32768
	ds_read_b128 v[106:109], v87 offset:34816
	ds_read_b128 v[110:113], v86 offset:36864
	ds_read_b128 v[114:117], v86 offset:38912
	ds_read_b128 v[118:121], v87 offset:36864
	ds_read_b128 v[122:125], v87 offset:38912
	buffer_load_dwordx4 v76, s[4:7], s53 offen lds
	s_mov_b32 m0, s35
	s_nop 0
	buffer_load_dwordx4 v78, s[4:7], s53 offen lds
	s_waitcnt vmcnt(8)
	s_waitcnt lgkmcnt(0)
	s_barrier
	s_waitcnt lgkmcnt(7)
	v_mfma_f32_16x16x32_bf16 v[60:63], v[64:67], v[94:97], v[60:63]
	v_mfma_f32_16x16x32_bf16 v[56:59], v[72:75], v[94:97], v[56:59]
	s_waitcnt lgkmcnt(6)
	v_mfma_f32_16x16x32_bf16 v[52:55], v[64:67], v[98:101], v[52:55]
	v_mfma_f32_16x16x32_bf16 v[48:51], v[72:75], v[98:101], v[48:51]
	s_waitcnt lgkmcnt(3)
	v_mfma_f32_16x16x32_bf16 v[44:47], v[64:67], v[110:113], v[44:47]
	v_mfma_f32_16x16x32_bf16 v[40:43], v[72:75], v[110:113], v[40:43]
	s_waitcnt lgkmcnt(2)
	v_mfma_f32_16x16x32_bf16 v[36:39], v[64:67], v[114:117], v[36:39]
	v_mfma_f32_16x16x32_bf16 v[32:35], v[72:75], v[114:117], v[32:35]
	v_mfma_f32_16x16x32_bf16 v[60:63], v[68:71], v[102:105], v[60:63]
	v_mfma_f32_16x16x32_bf16 v[56:59], v[90:93], v[102:105], v[56:59]
	v_mfma_f32_16x16x32_bf16 v[52:55], v[68:71], v[106:109], v[52:55]
	v_mfma_f32_16x16x32_bf16 v[48:51], v[90:93], v[106:109], v[48:51]
	s_waitcnt lgkmcnt(1)
	v_mfma_f32_16x16x32_bf16 v[44:47], v[68:71], v[118:121], v[44:47]
	v_mfma_f32_16x16x32_bf16 v[40:43], v[90:93], v[118:121], v[40:43]
	s_waitcnt lgkmcnt(0)
	v_mfma_f32_16x16x32_bf16 v[36:39], v[68:71], v[122:125], v[36:39]
	v_mfma_f32_16x16x32_bf16 v[32:35], v[90:93], v[122:125], v[32:35]
	s_barrier
	s_mov_b32 m0, s38
	s_or_b32 s53, s54, 0x80
	ds_read_b128 v[94:97], v86 offset:49152
	ds_read_b128 v[98:101], v86 offset:51200
	ds_read_b128 v[102:105], v87 offset:49152
	ds_read_b128 v[106:109], v87 offset:51200
	ds_read_b128 v[110:113], v86 offset:53248
	ds_read_b128 v[114:117], v86 offset:55296
	ds_read_b128 v[118:121], v87 offset:53248
	ds_read_b128 v[122:125], v87 offset:55296
	buffer_load_dwordx4 v77, s[4:7], s53 offen lds
	s_mov_b32 m0, s39
	s_add_i32 s54, s54, 0x80080
	buffer_load_dwordx4 v79, s[4:7], s53 offen lds
	s_mov_b32 m0, s42
	s_nop 0
	buffer_load_dwordx4 v77, s[4:7], s54 offen lds
	s_mov_b32 m0, s43
	s_nop 0
	buffer_load_dwordx4 v79, s[4:7], s54 offen lds
	s_mov_b32 m0, s40
	s_nop 0
	buffer_load_dwordx4 v76, s[4:7], s55 offen lds
	s_mov_b32 m0, s41
	s_nop 0
	buffer_load_dwordx4 v78, s[4:7], s55 offen lds
	s_waitcnt vmcnt(8)
	s_waitcnt lgkmcnt(0)
	s_barrier
	s_waitcnt lgkmcnt(7)
	v_mfma_f32_16x16x32_bf16 v[28:31], v[64:67], v[94:97], v[28:31]
	v_mfma_f32_16x16x32_bf16 v[24:27], v[72:75], v[94:97], v[24:27]
	s_waitcnt lgkmcnt(6)
	v_mfma_f32_16x16x32_bf16 v[20:23], v[64:67], v[98:101], v[20:23]
	v_mfma_f32_16x16x32_bf16 v[16:19], v[72:75], v[98:101], v[16:19]
	s_waitcnt lgkmcnt(3)
	v_mfma_f32_16x16x32_bf16 v[12:15], v[64:67], v[110:113], v[12:15]
	v_mfma_f32_16x16x32_bf16 v[8:11], v[72:75], v[110:113], v[8:11]
	s_waitcnt lgkmcnt(2)
	v_mfma_f32_16x16x32_bf16 v[4:7], v[64:67], v[114:117], v[4:7]
	v_mfma_f32_16x16x32_bf16 v[0:3], v[72:75], v[114:117], v[0:3]
	v_mfma_f32_16x16x32_bf16 v[28:31], v[68:71], v[102:105], v[28:31]
	v_mfma_f32_16x16x32_bf16 v[24:27], v[90:93], v[102:105], v[24:27]
	v_mfma_f32_16x16x32_bf16 v[20:23], v[68:71], v[106:109], v[20:23]
	v_mfma_f32_16x16x32_bf16 v[16:19], v[90:93], v[106:109], v[16:19]
	s_waitcnt lgkmcnt(1)
	v_mfma_f32_16x16x32_bf16 v[12:15], v[68:71], v[118:121], v[12:15]
	v_mfma_f32_16x16x32_bf16 v[8:11], v[90:93], v[118:121], v[8:11]
	s_waitcnt lgkmcnt(0)
	v_mfma_f32_16x16x32_bf16 v[4:7], v[68:71], v[122:125], v[4:7]
	v_mfma_f32_16x16x32_bf16 v[0:3], v[90:93], v[122:125], v[0:3]
	s_barrier
	s_add_i32 s52, s52, 2
	s_addk_i32 s2, 0x100
	s_addk_i32 s3, 0x100
	s_cmp_gt_u32 s52, 29
	s_cbranch_scc0 .LBB0_1102
	s_and_b64 vcc, exec, s[12:13]
	s_cbranch_vccz .LBB0_1105
	s_barrier

; #define PG8_STAGE(bufoff, gbase, voff) do { _Pragma("unroll") for (int _i = 0; _i < 2; ++_i) \
;         __builtin_amdgcn_raw_ptr_buffer_load_lds(rsrc, (LAS void*)(lds + (bufoff) + ldsw + _i * 8192), 16, (int)(voff)[_i], (int)(gbase), 0, 0); } while (0)
; #define PG8_STAGE_A(bufoff, h, goff) do { if constexpr (GATHER) { PG8_STAGE(bufoff, goff, vG[h]); } else { PG8_STAGE(bufoff, (goff) + (h) * hstep, voffA); } } while (0)
; #define PG8_WAIT_V(n) asm volatile("s_waitcnt vmcnt(" #n ")" ::: "memory")
; #define PG8_WAIT_L(n) asm volatile("s_waitcnt lgkmcnt(" #n ")" ::: "memory")
; #define PG8_BAR __builtin_amdgcn_s_barrier()
; #define PG8_SCHED __builtin_amdgcn_sched_barrier(0)
;     DI int row_cnt(const pg8::Unit& u) const { return __builtin_amdgcn_readfirstlane(tab[u.a0]) - u.ldc; }
;     ...
;             PG8_LDB(B0, 0, 0); PG8_LDB(B1, 0, 1); PG8_SCHED; PG8_LDA(At, 0, 0); PG8_STAGE_A(PG8_SA(1, 1), 1, a1);
;             if constexpr (GATHER) { if (last && has_next) load_rows((ui + 1) & 1, S.row_cnt(nxt)); }
;             PG8_WAIT_V(8); PG8_WAIT_L(0); PG8_BAR; PG8_MMA(0, 0, At, B0); PG8_MMA(0, 1, At, B1); PG8_BAR; PG8_SCHED;
;             PG8_LDA(At, 0, 1); PG8_STAGE(PG8_SB(0, 0), b2, voffB); PG8_STAGE(PG8_SB(0, 1), b2 + hstep, voffB); PG8_STAGE_A(PG8_SA(0, 0), 0, a2);
;             PG8_WAIT_V(8); PG8_WAIT_L(0); PG8_BAR; PG8_MMA(1, 0, At, B0); PG8_MMA(1, 1, At, B1); PG8_BAR; PG8_SCHED;
;             PG8_LDB(B0, 1, 0); PG8_LDB(B1, 1, 1); PG8_SCHED; PG8_LDA(At, 1, 0); PG8_STAGE_A(PG8_SA(0, 1), 1, a2);
;             PG8_WAIT_V(8); PG8_WAIT_L(0); PG8_BAR; PG8_MMA(0, 0, At, B0); PG8_MMA(0, 1, At, B1); PG8_BAR; PG8_SCHED;
;             PG8_LDA(At, 1, 1); PG8_STAGE(PG8_SB(1, 0), b3, voffB); PG8_STAGE(PG8_SB(1, 1), b3 + hstep, voffB); PG8_STAGE_A(PG8_SA(1, 0), 0, a3);
;             PG8_WAIT_V(8); PG8_WAIT_L(0); PG8_BAR; PG8_MMA(1, 0, At, B0); PG8_MMA(1, 1, At, B1); PG8_BAR; PG8_SCHED;
.LBB0_1242:
	s_add_i32 s4, s69, 0x80
	s_and_b64 s[2:3], s[28:29], exec
	s_cselect_b32 s70, 0x70e00000, s4
	s_add_i32 s2, s64, s69
	s_waitcnt vmcnt(8)
	s_add_i32 s3, s2, 0x8f200080
	s_or_b32 s2, s70, 0x80
	s_waitcnt lgkmcnt(0)
	s_and_b64 s[28:29], s[28:29], exec
	s_cselect_b32 s3, s62, s3
	s_add_i32 s28, s3, 0x80
	s_barrier
	s_waitcnt lgkmcnt(5)
	v_mfma_f32_16x16x128_f8f6f4 v[188:191], v[16:23], v[40:47], v[188:191]
	v_mfma_f32_16x16x128_f8f6f4 v[180:183], v[24:31], v[40:47], v[180:183]
	s_waitcnt lgkmcnt(4)
	v_mfma_f32_16x16x128_f8f6f4 v[172:175], v[16:23], v[32:39], v[172:175]
	v_mfma_f32_16x16x128_f8f6f4 v[164:167], v[24:31], v[32:39], v[164:167]
	s_waitcnt lgkmcnt(1)
	v_mfma_f32_16x16x128_f8f6f4 v[156:159], v[16:23], v[56:63], v[156:159]
	v_mfma_f32_16x16x128_f8f6f4 v[148:151], v[24:31], v[56:63], v[148:151]
	s_waitcnt lgkmcnt(0)
	v_mfma_f32_16x16x128_f8f6f4 v[140:143], v[16:23], v[48:55], v[140:143]
	v_mfma_f32_16x16x128_f8f6f4 v[132:135], v[24:31], v[48:55], v[132:135]
	v_mfma_f32_16x16x128_f8f6f4 v[184:187], v[0:7], v[40:47], v[184:187]
	v_mfma_f32_16x16x128_f8f6f4 v[176:179], v[8:15], v[40:47], v[176:179]
	v_mfma_f32_16x16x128_f8f6f4 v[168:171], v[0:7], v[32:39], v[168:171]
	v_mfma_f32_16x16x128_f8f6f4 v[160:163], v[8:15], v[32:39], v[160:163]
	v_mfma_f32_16x16x128_f8f6f4 v[152:155], v[0:7], v[56:63], v[152:155]
	v_mfma_f32_16x16x128_f8f6f4 v[144:147], v[8:15], v[56:63], v[144:147]
	v_mfma_f32_16x16x128_f8f6f4 v[136:139], v[0:7], v[48:55], v[136:139]
	v_mfma_f32_16x16x128_f8f6f4 v[128:131], v[8:15], v[48:55], v[128:131]
	s_barrier
	v_readlane_b32 s72, v254, 2
	v_readlane_b32 s74, v254, 4
	s_mov_b32 m0, s30
	s_mov_b32 s4, s74
	ds_read_b128 v[32:35], v204 offset:16384
	ds_read_b128 v[40:43], v204 offset:18432
	ds_read_b128 v[36:39], v205 offset:16384
	ds_read_b128 v[44:47], v205 offset:18432
	ds_read_b128 v[48:51], v204 offset:20480
	ds_read_b128 v[56:59], v204 offset:22528
	ds_read_b128 v[52:55], v205 offset:20480
	ds_read_b128 v[60:63], v205 offset:22528
	buffer_load_dwordx4 v192, s[4:7], s3 offen lds
	s_mov_b32 m0, s31
	s_add_i32 s29, s3, 0x40000
	buffer_load_dwordx4 v193, s[4:7], s3 offen lds
	s_mov_b32 m0, s33
	v_readlane_b32 s73, v254, 3
	buffer_load_dwordx4 v192, s[4:7], s29 offen lds
	s_mov_b32 m0, s34
	v_readlane_b32 s75, v254, 5
	buffer_load_dwordx4 v193, s[4:7], s29 offen lds
	s_mov_b32 m0, s21
	s_nop 0
	buffer_load_dwordx4 v196, s[4:7], s70 offen lds
	s_mov_b32 m0, s35
	s_nop 0
	buffer_load_dwordx4 v194, s[4:7], s70 offen lds
	s_waitcnt vmcnt(8)
	s_waitcnt lgkmcnt(0)
	s_barrier
	s_waitcnt lgkmcnt(5)
	v_mfma_f32_16x16x128_f8f6f4 v[124:127], v[16:23], v[32:39], v[124:127]
	v_mfma_f32_16x16x128_f8f6f4 v[116:119], v[24:31], v[32:39], v[116:119]
	s_waitcnt lgkmcnt(4)
	v_mfma_f32_16x16x128_f8f6f4 v[108:111], v[16:23], v[40:47], v[108:111]
	v_mfma_f32_16x16x128_f8f6f4 v[100:103], v[24:31], v[40:47], v[100:103]
	s_waitcnt lgkmcnt(1)
	v_mfma_f32_16x16x128_f8f6f4 v[92:95], v[16:23], v[48:55], v[92:95]
	v_mfma_f32_16x16x128_f8f6f4 v[84:87], v[24:31], v[48:55], v[84:87]
	s_waitcnt lgkmcnt(0)
	v_mfma_f32_16x16x128_f8f6f4 v[76:79], v[16:23], v[56:63], v[76:79]
	v_mfma_f32_16x16x128_f8f6f4 v[68:71], v[24:31], v[56:63], v[68:71]
	v_mfma_f32_16x16x128_f8f6f4 v[120:123], v[0:7], v[32:39], v[120:123]
	v_mfma_f32_16x16x128_f8f6f4 v[112:115], v[8:15], v[32:39], v[112:115]
	v_mfma_f32_16x16x128_f8f6f4 v[104:107], v[0:7], v[40:47], v[104:107]
	v_mfma_f32_16x16x128_f8f6f4 v[96:99], v[8:15], v[40:47], v[96:99]
	v_mfma_f32_16x16x128_f8f6f4 v[88:91], v[0:7], v[48:55], v[88:91]
	v_mfma_f32_16x16x128_f8f6f4 v[80:83], v[8:15], v[48:55], v[80:83]
	v_mfma_f32_16x16x128_f8f6f4 v[72:75], v[0:7], v[56:63], v[72:75]
	v_mfma_f32_16x16x128_f8f6f4 v[64:67], v[8:15], v[56:63], v[64:67]
	s_barrier
; #define PG8_STAGE(bufoff, gbase, voff) do { _Pragma("unroll") for (int _i = 0; _i < 2; ++_i) \
;         __builtin_amdgcn_raw_ptr_buffer_load_lds(rsrc, (LAS void*)(lds + (bufoff) + ldsw + _i * 8192), 16, (int)(voff)[_i], (int)(gbase), 0, 0); } while (0)
; #define PG8_STAGE_A(bufoff, h, goff) do { if constexpr (GATHER) { PG8_STAGE(bufoff, goff, vG[h]); } else { PG8_STAGE(bufoff, (goff) + (h) * hstep, voffA); } } while (0)
; #define PG8_WAIT_V(n) asm volatile("s_waitcnt vmcnt(" #n ")" ::: "memory")
; #define PG8_WAIT_L(n) asm volatile("s_waitcnt lgkmcnt(" #n ")" ::: "memory")
; #define PG8_BAR __builtin_amdgcn_s_barrier()
; #define PG8_SCHED __builtin_amdgcn_sched_barrier(0)
;     DI int row_cnt(const pg8::Unit& u) const { return __builtin_amdgcn_readfirstlane(tab[u.a0]) - u.ldc; }
;     ...
;             PG8_LDB(B0, 0, 0); PG8_LDB(B1, 0, 1); PG8_SCHED; PG8_LDA(At, 0, 0); PG8_STAGE_A(PG8_SA(1, 1), 1, a1);
;             if constexpr (GATHER) { if (last && has_next) load_rows((ui + 1) & 1, S.row_cnt(nxt)); }
;             PG8_WAIT_V(8); PG8_WAIT_L(0); PG8_BAR; PG8_MMA(0, 0, At, B0); PG8_MMA(0, 1, At, B1); PG8_BAR; PG8_SCHED;
;             PG8_LDA(At, 0, 1); PG8_STAGE(PG8_SB(0, 0), b2, voffB); PG8_STAGE(PG8_SB(0, 1), b2 + hstep, voffB); PG8_STAGE_A(PG8_SA(0, 0), 0, a2);
;             PG8_WAIT_V(8); PG8_WAIT_L(0); PG8_BAR; PG8_MMA(1, 0, At, B0); PG8_MMA(1, 1, At, B1); PG8_BAR; PG8_SCHED;
;             PG8_LDB(B0, 1, 0); PG8_LDB(B1, 1, 1); PG8_SCHED; PG8_LDA(At, 1, 0); PG8_STAGE_A(PG8_SA(0, 1), 1, a2);
;             PG8_WAIT_V(8); PG8_WAIT_L(0); PG8_BAR; PG8_MMA(0, 0, At, B0); PG8_MMA(0, 1, At, B1); PG8_BAR; PG8_SCHED;
;             PG8_LDA(At, 1, 1); PG8_STAGE(PG8_SB(1, 0), b3, voffB); PG8_STAGE(PG8_SB(1, 1), b3 + hstep, voffB); PG8_STAGE_A(PG8_SA(1, 0), 0, a3);
;             PG8_WAIT_V(8); PG8_WAIT_L(0); PG8_BAR; PG8_MMA(1, 0, At, B0); PG8_MMA(1, 1, At, B1); PG8_BAR; PG8_SCHED;
	s_add_i32 s29, 0, 0x18000
	v_add_u32_e32 v4, s29, v198
	v_add_u32_e32 v12, s29, v199
	s_add_i32 s29, 0, 0x1c000
	v_add_u32_e32 v20, s29, v198
	v_add_u32_e32 v28, s29, v199
	ds_read_b128 v[0:3], v4
	ds_read_b128 v[8:11], v4 offset:2048
	ds_read_b128 v[4:7], v12
	ds_read_b128 v[12:15], v12 offset:2048
	ds_read_b128 v[16:19], v20
	ds_read_b128 v[24:27], v20 offset:2048
	ds_read_b128 v[20:23], v28
	ds_read_b128 v[28:31], v28 offset:2048
	s_mov_b32 m0, s36
	ds_read_b128 v[32:35], v204 offset:32768
	ds_read_b128 v[40:43], v204 offset:34816
	ds_read_b128 v[36:39], v205 offset:32768
	ds_read_b128 v[44:47], v205 offset:34816
	ds_read_b128 v[48:51], v204 offset:36864
	ds_read_b128 v[56:59], v204 offset:38912
	ds_read_b128 v[52:55], v205 offset:36864
	ds_read_b128 v[60:63], v205 offset:38912
	buffer_load_dwordx4 v195, s[4:7], s70 offen lds
	s_mov_b32 m0, s37
	s_nop 0
	buffer_load_dwordx4 v197, s[4:7], s70 offen lds
	s_waitcnt vmcnt(8)
	s_waitcnt lgkmcnt(0)
	s_barrier
	s_waitcnt lgkmcnt(5)
	v_mfma_f32_16x16x128_f8f6f4 v[188:191], v[0:7], v[32:39], v[188:191]
	v_mfma_f32_16x16x128_f8f6f4 v[180:183], v[8:15], v[32:39], v[180:183]
	s_waitcnt lgkmcnt(4)
	v_mfma_f32_16x16x128_f8f6f4 v[172:175], v[0:7], v[40:47], v[172:175]
	v_mfma_f32_16x16x128_f8f6f4 v[164:167], v[8:15], v[40:47], v[164:167]
	s_waitcnt lgkmcnt(1)
	v_mfma_f32_16x16x128_f8f6f4 v[156:159], v[0:7], v[48:55], v[156:159]
	v_mfma_f32_16x16x128_f8f6f4 v[148:151], v[8:15], v[48:55], v[148:151]
	s_waitcnt lgkmcnt(0)
	v_mfma_f32_16x16x128_f8f6f4 v[140:143], v[0:7], v[56:63], v[140:143]
	v_mfma_f32_16x16x128_f8f6f4 v[132:135], v[8:15], v[56:63], v[132:135]
	v_mfma_f32_16x16x128_f8f6f4 v[184:187], v[16:23], v[32:39], v[184:187]
	v_mfma_f32_16x16x128_f8f6f4 v[176:179], v[24:31], v[32:39], v[176:179]
	v_mfma_f32_16x16x128_f8f6f4 v[168:171], v[16:23], v[40:47], v[168:171]
	v_mfma_f32_16x16x128_f8f6f4 v[160:163], v[24:31], v[40:47], v[160:163]
	v_mfma_f32_16x16x128_f8f6f4 v[152:155], v[16:23], v[48:55], v[152:155]
	v_mfma_f32_16x16x128_f8f6f4 v[144:147], v[24:31], v[48:55], v[144:147]
	v_mfma_f32_16x16x128_f8f6f4 v[136:139], v[16:23], v[56:63], v[136:139]
	v_mfma_f32_16x16x128_f8f6f4 v[128:131], v[24:31], v[56:63], v[128:131]
	s_barrier
	s_mov_b32 m0, s39
	ds_read_b128 v[32:35], v204 offset:49152
	ds_read_b128 v[40:43], v204 offset:51200
	ds_read_b128 v[36:39], v205 offset:49152
	ds_read_b128 v[44:47], v205 offset:51200
	ds_read_b128 v[48:51], v204 offset:53248
	ds_read_b128 v[56:59], v204 offset:55296
	ds_read_b128 v[52:55], v205 offset:53248
	ds_read_b128 v[60:63], v205 offset:55296
	buffer_load_dwordx4 v192, s[4:7], s28 offen lds
	s_mov_b32 m0, s40
	s_add_i32 s3, s3, 0x40080
	buffer_load_dwordx4 v193, s[4:7], s28 offen lds
	s_mov_b32 m0, s43
	s_nop 0
	buffer_load_dwordx4 v192, s[4:7], s3 offen lds
	s_mov_b32 m0, s44
	s_nop 0
	buffer_load_dwordx4 v193, s[4:7], s3 offen lds
	s_mov_b32 m0, s41
	s_nop 0
	buffer_load_dwordx4 v196, s[4:7], s2 offen lds
	s_mov_b32 m0, s42
	s_nop 0
	buffer_load_dwordx4 v194, s[4:7], s2 offen lds
	s_waitcnt vmcnt(8)
	s_waitcnt lgkmcnt(0)
	s_barrier
	s_waitcnt lgkmcnt(5)
	v_mfma_f32_16x16x128_f8f6f4 v[124:127], v[0:7], v[32:39], v[124:127]
	v_mfma_f32_16x16x128_f8f6f4 v[116:119], v[8:15], v[32:39], v[116:119]
	s_waitcnt lgkmcnt(4)
	v_mfma_f32_16x16x128_f8f6f4 v[108:111], v[0:7], v[40:47], v[108:111]
	v_mfma_f32_16x16x128_f8f6f4 v[100:103], v[8:15], v[40:47], v[100:103]
	s_waitcnt lgkmcnt(1)
	v_mfma_f32_16x16x128_f8f6f4 v[92:95], v[0:7], v[48:55], v[92:95]
	v_mfma_f32_16x16x128_f8f6f4 v[84:87], v[8:15], v[48:55], v[84:87]
	s_waitcnt lgkmcnt(0)
	v_mfma_f32_16x16x128_f8f6f4 v[76:79], v[0:7], v[56:63], v[76:79]
	v_mfma_f32_16x16x128_f8f6f4 v[68:71], v[8:15], v[56:63], v[68:71]
	v_mfma_f32_16x16x128_f8f6f4 v[120:123], v[16:23], v[32:39], v[120:123]
	v_mfma_f32_16x16x128_f8f6f4 v[112:115], v[24:31], v[32:39], v[112:115]
	v_mfma_f32_16x16x128_f8f6f4 v[104:107], v[16:23], v[40:47], v[104:107]
	v_mfma_f32_16x16x128_f8f6f4 v[96:99], v[24:31], v[40:47], v[96:99]
	v_mfma_f32_16x16x128_f8f6f4 v[88:91], v[16:23], v[48:55], v[88:91]
	v_mfma_f32_16x16x128_f8f6f4 v[80:83], v[24:31], v[48:55], v[80:83]
	v_mfma_f32_16x16x128_f8f6f4 v[72:75], v[16:23], v[56:63], v[72:75]
	v_mfma_f32_16x16x128_f8f6f4 v[64:67], v[24:31], v[56:63], v[64:67]
	s_barrier
	s_add_i32 s68, s68, 2
	s_addk_i32 s69, 0x100
	s_cmp_gt_u32 s68, 13
	s_cbranch_scc1 .LBB0_1252

; #define PG8_STAGE(bufoff, gbase, voff) do { _Pragma("unroll") for (int _i = 0; _i < 2; ++_i) \
;         __builtin_amdgcn_raw_ptr_buffer_load_lds(rsrc, (LAS void*)(lds + (bufoff) + ldsw + _i * 8192), 16, (int)(voff)[_i], (int)(gbase), 0, 0); } while (0)
; #define PG8_STAGE_A(bufoff, h, goff) do { if constexpr (GATHER) { PG8_STAGE(bufoff, goff, vG[h]); } else { PG8_STAGE(bufoff, (goff) + (h) * hstep, voffA); } } while (0)
; #define PG8_WAIT_V(n) asm volatile("s_waitcnt vmcnt(" #n ")" ::: "memory")
; #define PG8_WAIT_L(n) asm volatile("s_waitcnt lgkmcnt(" #n ")" ::: "memory")
; #define PG8_BAR __builtin_amdgcn_s_barrier()
; #define PG8_SCHED __builtin_amdgcn_sched_barrier(0)
;     DI int row_cnt(const pg8::Unit& u) const { return __builtin_amdgcn_readfirstlane(tab[u.a0]) - u.ldc; }
;     ...
;             PG8_LDB(B0, 0, 0); PG8_LDB(B1, 0, 1); PG8_SCHED; PG8_LDA(At, 0, 0); PG8_STAGE_A(PG8_SA(1, 1), 1, a1);
;             if constexpr (GATHER) { if (last && has_next) load_rows((ui + 1) & 1, S.row_cnt(nxt)); }
;             PG8_WAIT_V(8); PG8_WAIT_L(0); PG8_BAR; PG8_MMA(0, 0, At, B0); PG8_MMA(0, 1, At, B1); PG8_BAR; PG8_SCHED;
;             PG8_LDA(At, 0, 1); PG8_STAGE(PG8_SB(0, 0), b2, voffB); PG8_STAGE(PG8_SB(0, 1), b2 + hstep, voffB); PG8_STAGE_A(PG8_SA(0, 0), 0, a2);
;             PG8_WAIT_V(8); PG8_WAIT_L(0); PG8_BAR; PG8_MMA(1, 0, At, B0); PG8_MMA(1, 1, At, B1); PG8_BAR; PG8_SCHED;
;             PG8_LDB(B0, 1, 0); PG8_LDB(B1, 1, 1); PG8_SCHED; PG8_LDA(At, 1, 0); PG8_STAGE_A(PG8_SA(0, 1), 1, a2);
;             PG8_WAIT_V(8); PG8_WAIT_L(0); PG8_BAR; PG8_MMA(0, 0, At, B0); PG8_MMA(0, 1, At, B1); PG8_BAR; PG8_SCHED;
;             PG8_LDA(At, 1, 1); PG8_STAGE(PG8_SB(1, 0), b3, voffB); PG8_STAGE(PG8_SB(1, 1), b3 + hstep, voffB); PG8_STAGE_A(PG8_SA(1, 0), 0, a3);
;             PG8_WAIT_V(8); PG8_WAIT_L(0); PG8_BAR; PG8_MMA(1, 0, At, B0); PG8_MMA(1, 1, At, B1); PG8_BAR; PG8_SCHED;
.LBB0_1335:
	s_waitcnt vmcnt(1)
	ds_read_b128 v[128:131], v152
	ds_read_b128 v[136:139], v152 offset:2048
	s_waitcnt vmcnt(0)
	ds_read_b128 v[132:135], v153
	ds_read_b128 v[140:143], v153 offset:2048
	ds_read_b128 v[158:161], v154
	ds_read_b128 v[166:169], v154 offset:2048
	ds_read_b128 v[162:165], v155
	ds_read_b128 v[170:173], v155 offset:2048
	s_add_i32 s4, s3, 0xfffc0080
	s_cmp_eq_u32 s54, 12
	s_cselect_b32 s57, s52, s4
	s_cselect_b32 s56, s51, s53
	s_add_i32 s55, s57, 0x80
	s_mov_b32 s4, s62
	s_mov_b32 m0, s41
	ds_read_b128 v[174:177], v156
	ds_read_b128 v[182:185], v156 offset:2048
	ds_read_b128 v[178:181], v157
	ds_read_b128 v[186:189], v157 offset:2048
	ds_read_b128 v[190:193], v156 offset:4096
	ds_read_b128 v[198:201], v156 offset:6144
	ds_read_b128 v[194:197], v157 offset:4096
	ds_read_b128 v[202:205], v157 offset:6144
	buffer_load_dwordx4 v146, s[4:7], s3 offen lds
	s_mov_b32 m0, s44
	s_nop 0
	buffer_load_dwordx4 v148, s[4:7], s3 offen lds
	s_waitcnt vmcnt(8)
	s_waitcnt lgkmcnt(0)
	s_barrier
	s_waitcnt lgkmcnt(5)
	v_mfma_f32_16x16x128_f8f6f4 v[124:127], v[128:135], v[174:181], v[124:127]
	v_mfma_f32_16x16x128_f8f6f4 v[120:123], v[136:143], v[174:181], v[120:123]
	s_waitcnt lgkmcnt(4)
	v_mfma_f32_16x16x128_f8f6f4 v[108:111], v[128:135], v[182:189], v[108:111]
	v_mfma_f32_16x16x128_f8f6f4 v[104:107], v[136:143], v[182:189], v[104:107]
	s_waitcnt lgkmcnt(1)
	v_mfma_f32_16x16x128_f8f6f4 v[206:209], v[128:135], v[190:197], v[92:95]
	v_mfma_f32_16x16x128_f8f6f4 v[210:213], v[136:143], v[190:197], v[88:91]
	s_waitcnt lgkmcnt(0)
	v_mfma_f32_16x16x128_f8f6f4 v[214:217], v[128:135], v[198:205], v[76:79]
	v_mfma_f32_16x16x128_f8f6f4 v[218:221], v[136:143], v[198:205], v[72:75]
	v_mfma_f32_16x16x128_f8f6f4 v[116:119], v[158:165], v[174:181], v[116:119]
	v_mfma_f32_16x16x128_f8f6f4 v[112:115], v[166:173], v[174:181], v[112:115]
	v_mfma_f32_16x16x128_f8f6f4 v[100:103], v[158:165], v[182:189], v[100:103]
	v_mfma_f32_16x16x128_f8f6f4 v[96:99], v[166:173], v[182:189], v[96:99]
	v_mfma_f32_16x16x128_f8f6f4 v[174:177], v[158:165], v[190:197], v[84:87]
	v_mfma_f32_16x16x128_f8f6f4 v[178:181], v[166:173], v[190:197], v[80:83]
	v_mfma_f32_16x16x128_f8f6f4 v[182:185], v[158:165], v[198:205], v[68:71]
	v_mfma_f32_16x16x128_f8f6f4 v[186:189], v[166:173], v[198:205], v[64:67]
	s_barrier
	s_mov_b32 m0, s24
	s_nop 3
	ds_read_b128 v[64:67], v156 offset:16384
	ds_read_b128 v[72:75], v156 offset:18432
	ds_read_b128 v[68:71], v157 offset:16384
	ds_read_b128 v[76:79], v157 offset:18432
	ds_read_b128 v[80:83], v156 offset:20480
	ds_read_b128 v[88:91], v156 offset:22528
	ds_read_b128 v[84:87], v157 offset:20480
	ds_read_b128 v[92:95], v157 offset:22528
	buffer_load_dwordx4 v147, s[4:7], s56 offen lds
	s_mov_b32 m0, s25
	s_add_i32 s58, s56, 0x40000
	buffer_load_dwordx4 v149, s[4:7], s56 offen lds
	s_mov_b32 m0, s26
	s_nop 0
	buffer_load_dwordx4 v147, s[4:7], s58 offen lds
	s_mov_b32 m0, s27
	s_nop 0
	buffer_load_dwordx4 v149, s[4:7], s58 offen lds
	s_mov_b32 m0, s17
	s_nop 0
	buffer_load_dwordx4 v146, s[4:7], s57 offen lds
	s_mov_b32 m0, s28
	s_nop 0
	buffer_load_dwordx4 v148, s[4:7], s57 offen lds
	s_waitcnt vmcnt(8)
	s_waitcnt lgkmcnt(0)
	s_barrier
	s_waitcnt lgkmcnt(5)
	v_mfma_f32_16x16x128_f8f6f4 v[60:63], v[128:135], v[64:71], v[60:63]
	v_mfma_f32_16x16x128_f8f6f4 v[56:59], v[136:143], v[64:71], v[56:59]
	s_waitcnt lgkmcnt(4)
	v_mfma_f32_16x16x128_f8f6f4 v[190:193], v[128:135], v[72:79], v[44:47]
	v_mfma_f32_16x16x128_f8f6f4 v[194:197], v[136:143], v[72:79], v[40:43]
	s_waitcnt lgkmcnt(1)
	v_mfma_f32_16x16x128_f8f6f4 v[198:201], v[128:135], v[80:87], v[28:31]
	v_mfma_f32_16x16x128_f8f6f4 v[202:205], v[136:143], v[80:87], v[24:27]
	s_waitcnt lgkmcnt(0)
	v_mfma_f32_16x16x128_f8f6f4 v[222:225], v[128:135], v[88:95], v[12:15]
	v_mfma_f32_16x16x128_f8f6f4 v[226:229], v[136:143], v[88:95], v[8:11]
	v_mfma_f32_16x16x128_f8f6f4 v[52:55], v[158:165], v[64:71], v[52:55]
	v_mfma_f32_16x16x128_f8f6f4 v[48:51], v[166:173], v[64:71], v[48:51]
	v_mfma_f32_16x16x128_f8f6f4 v[230:233], v[158:165], v[72:79], v[36:39]
	v_mfma_f32_16x16x128_f8f6f4 v[234:237], v[166:173], v[72:79], v[32:35]
	v_mfma_f32_16x16x128_f8f6f4 v[238:241], v[158:165], v[80:87], v[20:23]
	v_mfma_f32_16x16x128_f8f6f4 v[242:245], v[166:173], v[80:87], v[16:19]
	v_mfma_f32_16x16x128_f8f6f4 v[246:249], v[158:165], v[88:95], v[4:7]
	v_mfma_f32_16x16x128_f8f6f4 v[250:253], v[166:173], v[88:95], v[0:3]
	s_barrier
; #define PG8_STAGE(bufoff, gbase, voff) do { _Pragma("unroll") for (int _i = 0; _i < 2; ++_i) \
;         __builtin_amdgcn_raw_ptr_buffer_load_lds(rsrc, (LAS void*)(lds + (bufoff) + ldsw + _i * 8192), 16, (int)(voff)[_i], (int)(gbase), 0, 0); } while (0)
; #define PG8_STAGE_A(bufoff, h, goff) do { if constexpr (GATHER) { PG8_STAGE(bufoff, goff, vG[h]); } else { PG8_STAGE(bufoff, (goff) + (h) * hstep, voffA); } } while (0)
; #define PG8_WAIT_V(n) asm volatile("s_waitcnt vmcnt(" #n ")" ::: "memory")
; #define PG8_WAIT_L(n) asm volatile("s_waitcnt lgkmcnt(" #n ")" ::: "memory")
; #define PG8_BAR __builtin_amdgcn_s_barrier()
; #define PG8_SCHED __builtin_amdgcn_sched_barrier(0)
;     DI int row_cnt(const pg8::Unit& u) const { return __builtin_amdgcn_readfirstlane(tab[u.a0]) - u.ldc; }
;     ...
;             PG8_LDB(B0, 0, 0); PG8_LDB(B1, 0, 1); PG8_SCHED; PG8_LDA(At, 0, 0); PG8_STAGE_A(PG8_SA(1, 1), 1, a1);
;             if constexpr (GATHER) { if (last && has_next) load_rows((ui + 1) & 1, S.row_cnt(nxt)); }
;             PG8_WAIT_V(8); PG8_WAIT_L(0); PG8_BAR; PG8_MMA(0, 0, At, B0); PG8_MMA(0, 1, At, B1); PG8_BAR; PG8_SCHED;
;             PG8_LDA(At, 0, 1); PG8_STAGE(PG8_SB(0, 0), b2, voffB); PG8_STAGE(PG8_SB(0, 1), b2 + hstep, voffB); PG8_STAGE_A(PG8_SA(0, 0), 0, a2);
;             PG8_WAIT_V(8); PG8_WAIT_L(0); PG8_BAR; PG8_MMA(1, 0, At, B0); PG8_MMA(1, 1, At, B1); PG8_BAR; PG8_SCHED;
;             PG8_LDB(B0, 1, 0); PG8_LDB(B1, 1, 1); PG8_SCHED; PG8_LDA(At, 1, 0); PG8_STAGE_A(PG8_SA(0, 1), 1, a2);
;             PG8_WAIT_V(8); PG8_WAIT_L(0); PG8_BAR; PG8_MMA(0, 0, At, B0); PG8_MMA(0, 1, At, B1); PG8_BAR; PG8_SCHED;
;             PG8_LDA(At, 1, 1); PG8_STAGE(PG8_SB(1, 0), b3, voffB); PG8_STAGE(PG8_SB(1, 1), b3 + hstep, voffB); PG8_STAGE_A(PG8_SA(1, 0), 0, a3);
;             PG8_WAIT_V(8); PG8_WAIT_L(0); PG8_BAR; PG8_MMA(1, 0, At, B0); PG8_MMA(1, 1, At, B1); PG8_BAR; PG8_SCHED;
	s_add_i32 s58, 0, 0x18000
	s_nop 2
	v_add_u32_e32 v4, s58, v150
	v_add_u32_e32 v8, s58, v151
	s_add_i32 s58, 0, 0x1c000
	ds_read_b128 v[0:3], v4
	ds_read_b128 v[16:19], v4 offset:2048
	ds_read_b128 v[4:7], v8
	ds_read_b128 v[20:23], v8 offset:2048
	v_add_u32_e32 v8, s58, v150
	v_add_u32_e32 v9, s58, v151
	ds_read_b128 v[128:131], v8
	ds_read_b128 v[136:139], v8 offset:2048
	ds_read_b128 v[132:135], v9
	ds_read_b128 v[140:143], v9 offset:2048
	s_add_i32 s57, s57, 0x40000
	s_mov_b32 m0, s29
	ds_read_b128 v[8:11], v156 offset:32768
	ds_read_b128 v[24:27], v156 offset:34816
	ds_read_b128 v[12:15], v157 offset:32768
	ds_read_b128 v[28:31], v157 offset:34816
	ds_read_b128 v[32:35], v156 offset:36864
	ds_read_b128 v[40:43], v156 offset:38912
	ds_read_b128 v[36:39], v157 offset:36864
	ds_read_b128 v[44:47], v157 offset:38912
	buffer_load_dwordx4 v146, s[4:7], s57 offen lds
	s_mov_b32 m0, s31
	s_nop 0
	buffer_load_dwordx4 v148, s[4:7], s57 offen lds
	s_waitcnt vmcnt(8)
	s_waitcnt lgkmcnt(0)
	s_barrier
	s_waitcnt lgkmcnt(5)
	v_mfma_f32_16x16x128_f8f6f4 v[124:127], v[0:7], v[8:15], v[124:127]
	v_mfma_f32_16x16x128_f8f6f4 v[120:123], v[16:23], v[8:15], v[120:123]
	s_waitcnt lgkmcnt(4)
	v_mfma_f32_16x16x128_f8f6f4 v[108:111], v[0:7], v[24:31], v[108:111]
	v_mfma_f32_16x16x128_f8f6f4 v[104:107], v[16:23], v[24:31], v[104:107]
	s_waitcnt lgkmcnt(1)
	v_mfma_f32_16x16x128_f8f6f4 v[92:95], v[0:7], v[32:39], v[206:209]
	v_mfma_f32_16x16x128_f8f6f4 v[88:91], v[16:23], v[32:39], v[210:213]
	s_waitcnt lgkmcnt(0)
	v_mfma_f32_16x16x128_f8f6f4 v[76:79], v[0:7], v[40:47], v[214:217]
	v_mfma_f32_16x16x128_f8f6f4 v[72:75], v[16:23], v[40:47], v[218:221]
	v_mfma_f32_16x16x128_f8f6f4 v[116:119], v[128:135], v[8:15], v[116:119]
	v_mfma_f32_16x16x128_f8f6f4 v[112:115], v[136:143], v[8:15], v[112:115]
	v_mfma_f32_16x16x128_f8f6f4 v[100:103], v[128:135], v[24:31], v[100:103]
	v_mfma_f32_16x16x128_f8f6f4 v[96:99], v[136:143], v[24:31], v[96:99]
	v_mfma_f32_16x16x128_f8f6f4 v[84:87], v[128:135], v[32:39], v[174:177]
	v_mfma_f32_16x16x128_f8f6f4 v[80:83], v[136:143], v[32:39], v[178:181]
	v_mfma_f32_16x16x128_f8f6f4 v[68:71], v[128:135], v[40:47], v[182:185]
	v_mfma_f32_16x16x128_f8f6f4 v[64:67], v[136:143], v[40:47], v[186:189]
	s_barrier
	s_mov_b32 m0, s33
	s_add_i32 s57, s56, 0x80
	ds_read_b128 v[32:35], v156 offset:49152
	ds_read_b128 v[158:161], v156 offset:51200
	ds_read_b128 v[36:39], v157 offset:49152
	ds_read_b128 v[162:165], v157 offset:51200
	ds_read_b128 v[166:169], v156 offset:53248
	ds_read_b128 v[174:177], v156 offset:55296
	ds_read_b128 v[170:173], v157 offset:53248
	ds_read_b128 v[178:181], v157 offset:55296
	buffer_load_dwordx4 v147, s[4:7], s57 offen lds
	s_mov_b32 m0, s34
	s_add_i32 s56, s56, 0x40080
	buffer_load_dwordx4 v149, s[4:7], s57 offen lds
	s_mov_b32 m0, s37
	s_nop 0
	buffer_load_dwordx4 v147, s[4:7], s56 offen lds
	s_mov_b32 m0, s38
	s_nop 0
	buffer_load_dwordx4 v149, s[4:7], s56 offen lds
	s_mov_b32 m0, s35
	s_nop 0
	buffer_load_dwordx4 v146, s[4:7], s55 offen lds
	s_mov_b32 m0, s36
	s_nop 0
	buffer_load_dwordx4 v148, s[4:7], s55 offen lds
	s_waitcnt vmcnt(8)
	s_waitcnt lgkmcnt(0)
	s_barrier
	s_waitcnt lgkmcnt(5)
	v_mfma_f32_16x16x128_f8f6f4 v[60:63], v[0:7], v[32:39], v[60:63]
	v_mfma_f32_16x16x128_f8f6f4 v[56:59], v[16:23], v[32:39], v[56:59]
	s_waitcnt lgkmcnt(4)
	v_mfma_f32_16x16x128_f8f6f4 v[44:47], v[0:7], v[158:165], v[190:193]
	v_mfma_f32_16x16x128_f8f6f4 v[40:43], v[16:23], v[158:165], v[194:197]
	s_waitcnt lgkmcnt(1)
	v_mfma_f32_16x16x128_f8f6f4 v[28:31], v[0:7], v[166:173], v[198:201]
	v_mfma_f32_16x16x128_f8f6f4 v[24:27], v[16:23], v[166:173], v[202:205]
	s_waitcnt lgkmcnt(0)
	v_mfma_f32_16x16x128_f8f6f4 v[12:15], v[0:7], v[174:181], v[222:225]
	v_mfma_f32_16x16x128_f8f6f4 v[8:11], v[16:23], v[174:181], v[226:229]
	v_mfma_f32_16x16x128_f8f6f4 v[52:55], v[128:135], v[32:39], v[52:55]
	v_mfma_f32_16x16x128_f8f6f4 v[48:51], v[136:143], v[32:39], v[48:51]
	v_mfma_f32_16x16x128_f8f6f4 v[36:39], v[128:135], v[158:165], v[230:233]
	v_mfma_f32_16x16x128_f8f6f4 v[32:35], v[136:143], v[158:165], v[234:237]
	v_mfma_f32_16x16x128_f8f6f4 v[20:23], v[128:135], v[166:173], v[238:241]
	v_mfma_f32_16x16x128_f8f6f4 v[16:19], v[136:143], v[166:173], v[242:245]
	v_mfma_f32_16x16x128_f8f6f4 v[4:7], v[128:135], v[174:181], v[246:249]
	v_mfma_f32_16x16x128_f8f6f4 v[0:3], v[136:143], v[174:181], v[250:253]
	s_barrier
	s_add_i32 s54, s54, 2
	s_addk_i32 s3, 0x100
	s_addk_i32 s53, 0x100
	s_cmp_gt_u32 s54, 13
	s_cbranch_scc0 .LBB0_1335
	s_and_b64 vcc, exec, s[14:15]
	s_cbranch_vccz .LBB0_1338
	s_barrier
